# BEST + one static priority raise for waves 4-7 (the staggered half) instead of per-segment s_setprio toggles in all five K-loops
# speedup vs baseline: 1.0038x; 1.0004x over previous
; #define LAS __attribute__((address_space(3)))
; __device__ __forceinline__ unsigned xb_add(unsigned* p, unsigned v) { return __hip_atomic_fetch_add(p, v, __ATOMIC_RELAXED, __HIP_MEMORY_SCOPE_AGENT); }
; __device__ __forceinline__ unsigned xb_xcc_id() { return (unsigned)__builtin_amdgcn_s_getreg((3 << 11) | 20) & 0xFu; }
; __device__ __forceinline__ XcdBarrier xcd_barrier_post(unsigned* bar, volatile LAS unsigned* st) {
;     XcdBarrier b; b.bar = bar; b.x = xb_xcc_id(); b.st = st;
;     if (threadIdx.x == 0) (void)xb_add(&bar[XB_XCNT(b.x)], 1u);
;     return b;
; __global__ void __launch_bounds__(NTHREADS, 2) hymba_fwd(Params P) {
;     extern __shared__ __attribute__((aligned(16))) unsigned char lds_raw[];
;     LAS unsigned char* lds = (LAS unsigned char*)lds_raw;
;     const int tid = threadIdx.x, blk = blockIdx.x, G = gridDim.x;
;     volatile LAS unsigned* misc = (volatile LAS unsigned*)(lds + LDS_MISC);
;     if (tid < 64) misc[tid] = 0u;
;     __syncthreads();
;     XcdBarrier bar = xcd_barrier_post((unsigned*)(P.ws + WS_BAR), misc);
_Z9hymba_fwd6Params:
	v_readfirstlane_b32 s3, v0
	s_nop 3
	s_cmpk_lt_u32 s3, 0x100
	s_cbranch_scc1 .Lprio_lo
	s_setprio 1
.Lprio_lo:
	s_load_dwordx8 s[16:23], s[0:1], 0xc0
	s_load_dwordx4 s[12:15], s[0:1], 0xe0
	s_load_dword s33, s[0:1], 0xf0
	s_add_u32 s4, s0, 0xf0
	s_addc_u32 s5, s1, 0
	v_cmp_gt_u32_e64 s[6:7], 64, v0
	v_writelane_b32 v254, s4, 0
	s_nop 1
	v_writelane_b32 v254, s5, 1
	s_mov_b64 s[4:5], exec
	v_writelane_b32 v254, s6, 2
	s_nop 1
	v_writelane_b32 v254, s7, 3
	s_and_b64 s[6:7], s[4:5], s[6:7]
	s_mov_b64 exec, s[6:7]
	v_lshl_add_u32 v1, v0, 2, 0
	v_add_u32_e32 v1, 0x26000, v1
	v_mov_b32_e32 v2, 0
	ds_write_b32 v1, v2
	s_or_b64 exec, exec, s[4:5]
	s_waitcnt lgkmcnt(0)
	s_barrier
	s_getreg_b32 s3, hwreg(HW_REG_XCC_ID, 0, 4)
	s_and_b32 s3, s3, 15
	v_writelane_b32 v254, s3, 4
	v_cmp_eq_u32_e64 s[6:7], 0, v0
	s_mov_b64 s[4:5], exec
	s_nop 0
	v_writelane_b32 v254, s6, 5
	s_nop 1
	v_writelane_b32 v254, s7, 6
	s_and_b64 s[6:7], s[4:5], s[6:7]
	s_mov_b64 exec, s[6:7]
	s_cbranch_execz .LBB0_5
	s_mov_b64 s[6:7], exec
	v_mbcnt_lo_u32_b32 v1, s6, 0
	v_mbcnt_hi_u32_b32 v1, s7, v1
	v_cmp_eq_u32_e32 vcc, 0, v1
	s_and_b64 s[8:9], exec, vcc
	s_mov_b64 exec, s[8:9]
	s_cbranch_execz .LBB0_5
	v_readlane_b32 s3, v254, 4
	s_lshl_b32 s3, s3, 8
	s_bcnt1_i32_b64 s6, s[6:7]
	v_mov_b32_e32 v1, s3
	v_mov_b32_e32 v2, s6
	global_atomic_add v1, v2, s[12:13] offset:1024

; #define G8_STAGE(bufoff, gbase, v0, v1) do { unsigned x0_ = (v0), x1_ = (v1); asm volatile("" : "+v"(x0_), "+v"(x1_));     \
;         __builtin_amdgcn_global_load_lds((const unsigned*)((gbase) + x0_), (LAS unsigned*)(lds + (bufoff) + ldsw), 16, 0, 0); \
;         __builtin_amdgcn_global_load_lds((const unsigned*)((gbase) + x1_), (LAS unsigned*)(lds + (bufoff) + ldsw + 8192), 16, 0, 0); } while (0)
; #define G8_LDA(dst, b, h) do { _Pragma("unroll") for (int m = 0; m < 4; ++m) _Pragma("unroll") for (int k = 0; k < 2; ++k) dst[m][k] = *(const LAS bf16x8*)(lds + G8_SA(b, h) + aoff + m * 2048 + k * 1024); } while (0)
; #define G8_LDB(dst, b, h) do { _Pragma("unroll") for (int n = 0; n < 2; ++n) _Pragma("unroll") for (int k = 0; k < 2; ++k) dst[n][k] = *(const LAS bf16x8*)(lds + G8_SB(b, h) + boff + n * 2048 + k * 1024); } while (0)
; #define G8_WAIT_L(n) asm volatile("s_waitcnt lgkmcnt(" #n ")" ::: "memory")
; #define G8_BAR __builtin_amdgcn_s_barrier()
; #define G8_SCHED __builtin_amdgcn_sched_barrier(0)
;     ...
;             G8_CONV_READ; G8_SCHED;
;             G8_LDB(B0, 0, 0); G8_SCHED; G8_LDA(At, 0, 0); G8_STAGE(G8_SA(1, 1), a1, cv[1][0], cv[1][1]);
;             G8_WAIT_L(8); G8_BAR; G8_WAIT_L(0); if (do0) G8_MMA(0, 0, At, B0); G8_CONV_CVT; G8_BAR; G8_SCHED;
;             G8_LDB(B1, 0, 1); G8_STAGE(G8_SB(0, 0), b2, voffB[0], voffB[1]);
;             G8_BAR; G8_CONV_ISSUE;
.LBB0_234:
	s_add_u32 s4, s0, 0x80
	s_addc_u32 s5, s1, 0
	s_add_u32 s42, s0, 0x100
	s_addc_u32 s43, s1, 0
	s_add_u32 s49, s6, 0x10000
	s_addc_u32 s62, s7, 0
	s_cmp_eq_u32 s61, 28
	s_cselect_b32 s47, s69, s43
	s_cselect_b32 s46, s76, s42
	s_cselect_b32 s43, s57, s62
	s_cselect_b32 s42, s60, s49
	s_mov_b32 s49, 0
	s_nop 0
	v_mbcnt_lo_u32_b32 v130, -1, s49
	v_mbcnt_hi_u32_b32 v130, -1, v130
	v_and_b32_e32 v131, 15, v130
	v_lshrrev_b32_e32 v130, 2, v130
	v_mul_u32_u24_e32 v131, 0x410, v131
	v_and_b32_e32 v130, 0x3ffffffc, v130
	v_add3_u32 v130, s96, v131, v130
	ds_read2_b32 v[146:147], v130 offset1:32
	ds_read2_b32 v[148:149], v130 offset0:64 offset1:96
	ds_read2_b32 v[212:213], v130 offset0:128 offset1:160
	ds_read2_b32 v[214:215], v130 offset0:192 offset1:224
	s_add_i32 s49, 0, 0x10000
	v_add_u32_e32 v142, s49, v209
	ds_read_b128 v[130:133], v142
	ds_read_b128 v[134:137], v142 offset:1024
	ds_read_b128 v[138:141], v142 offset:2048
	ds_read_b128 v[142:145], v142 offset:3072
	v_mov_b32_e32 v150, v204
	v_mov_b32_e32 v151, v203
	s_add_i32 m0, s78, 0xc000
	ds_read_b128 v[186:189], v210
	ds_read_b128 v[190:193], v210 offset:1024
	ds_read_b128 v[178:181], v210 offset:2048
	ds_read_b128 v[182:185], v210 offset:3072
	ds_read_b128 v[170:173], v210 offset:4096
	ds_read_b128 v[174:177], v210 offset:5120
	ds_read_b128 v[162:165], v210 offset:6144
	ds_read_b128 v[166:169], v210 offset:7168
	s_nop 0
	global_load_lds_dwordx4 v151, s[4:5]
	s_add_i32 m0, s78, 0xe000
	s_nop 0
	global_load_lds_dwordx4 v150, s[4:5]
	s_waitcnt lgkmcnt(8)
	s_barrier
	s_waitcnt lgkmcnt(0)
	s_nop 0
	s_waitcnt lgkmcnt(0)
	v_mfma_f32_16x16x32_bf16 v[126:129], v[130:133], v[186:189], v[126:129]
	v_mfma_f32_16x16x32_bf16 v[122:125], v[138:141], v[186:189], v[122:125]
	v_mfma_f32_16x16x32_bf16 v[118:121], v[130:133], v[178:181], v[118:121]
	v_mfma_f32_16x16x32_bf16 v[114:117], v[138:141], v[178:181], v[114:117]
	v_mfma_f32_16x16x32_bf16 v[110:113], v[130:133], v[170:173], v[110:113]
	v_mfma_f32_16x16x32_bf16 v[106:109], v[138:141], v[170:173], v[106:109]
	v_mfma_f32_16x16x32_bf16 v[102:105], v[130:133], v[162:165], v[102:105]
	v_mfma_f32_16x16x32_bf16 v[98:101], v[138:141], v[162:165], v[98:101]
	v_mfma_f32_16x16x32_bf16 v[126:129], v[134:137], v[190:193], v[126:129]
	v_mfma_f32_16x16x32_bf16 v[122:125], v[142:145], v[190:193], v[122:125]
	v_mfma_f32_16x16x32_bf16 v[118:121], v[134:137], v[182:185], v[118:121]
	v_mfma_f32_16x16x32_bf16 v[114:117], v[142:145], v[182:185], v[114:117]
	v_mfma_f32_16x16x32_bf16 v[110:113], v[134:137], v[174:177], v[110:113]
	v_mfma_f32_16x16x32_bf16 v[106:109], v[142:145], v[174:177], v[106:109]
	v_mfma_f32_16x16x32_bf16 v[102:105], v[134:137], v[166:169], v[102:105]
	v_mfma_f32_16x16x32_bf16 v[98:101], v[142:145], v[166:169], v[98:101]
	s_nop 0
	v_mul_f32_e32 v146, s59, v146
	v_mul_f32_e32 v147, s59, v147
	v_mov_b32_e32 v216, 0
	v_cvt_pk_fp8_f32 v216, v146, v147
	v_mul_f32_e32 v146, s59, v148
	v_mul_f32_e32 v147, s59, v149
	v_mul_f32_e32 v194, s59, v213
	v_cvt_pk_fp8_f32 v216, v146, v147 op_sel:[0,0,1]
	v_mul_f32_e32 v213, s59, v215
	s_barrier
	v_mul_f32_e32 v212, s59, v212
	v_mov_b32_e32 v217, 0
	v_cvt_pk_fp8_f32 v217, v212, v194
	v_mul_f32_e32 v194, s59, v214
	s_add_i32 s4, s49, s77
	v_mov_b32_e32 v212, v198
	v_cvt_pk_fp8_f32 v217, v194, v213 op_sel:[0,0,1]
	v_mov_b32_e32 v194, v1
	s_mov_b32 m0, s4
	ds_read_b128 v[146:149], v211
	ds_read_b128 v[150:153], v211 offset:1024
	ds_read_b128 v[154:157], v211 offset:2048
	ds_read_b128 v[158:161], v211 offset:3072
	s_min_i32 s62, s68, s52
	global_load_lds_dwordx4 v194, s[42:43]
	s_add_i32 m0, s4, 0x2000
	s_mov_b32 s4, 0
	global_load_lds_dwordx4 v212, s[42:43]
	s_barrier
	s_ashr_i32 s64, s62, 2
	v_mbcnt_lo_u32_b32 v194, -1, s4
	v_mbcnt_hi_u32_b32 v194, -1, v194
	v_lshlrev_b32_e32 v212, 3, v194
	v_and_b32_e32 v213, 0xffffff80, v212
	v_add_u32_e32 v213, s97, v213
	s_movk_i32 s4, 0x78
	v_and_or_b32 v212, v212, s4, v213
	s_cmp_eq_u32 s64, s48
	global_store_dwordx2 v212, v[216:217], s[40:41] nt
	s_cbranch_scc1 .LBB0_241
	s_mul_i32 s41, s64, s33
	s_add_i32 s41, s41, s2
	s_cmpk_gt_i32 s41, 0x1fff
	s_mov_b64 s[48:49], -1
	s_cbranch_scc0 .LBB0_237
	s_add_i32 s4, s41, 0xffffe000
	s_lshr_b32 s14, s4, 7
	s_lshl_b64 s[4:5], s[14:15], 23
	s_add_u32 s28, s18, s4
	s_addc_u32 s29, s19, s5
	s_lshl_b64 s[4:5], s[14:15], 21
	s_add_u32 s30, s53, s4
	s_addc_u32 s31, s54, s5
	s_lshl_b32 s4, s41, 3
	s_and_b32 s67, s4, 0x380
	s_lshl_b32 s4, s41, 7
	s_and_b32 s40, s4, 0x780
	s_mov_b64 s[48:49], 0

; #define G8_STAGE(bufoff, gbase, v0, v1) do { unsigned x0_ = (v0), x1_ = (v1); asm volatile("" : "+v"(x0_), "+v"(x1_));     \
;         __builtin_amdgcn_global_load_lds((const unsigned*)((gbase) + x0_), (LAS unsigned*)(lds + (bufoff) + ldsw), 16, 0, 0); \
;         __builtin_amdgcn_global_load_lds((const unsigned*)((gbase) + x1_), (LAS unsigned*)(lds + (bufoff) + ldsw + 8192), 16, 0, 0); } while (0)
; #define G8_LDA(dst, b, h) do { _Pragma("unroll") for (int m = 0; m < 4; ++m) _Pragma("unroll") for (int k = 0; k < 2; ++k) dst[m][k] = *(const LAS bf16x8*)(lds + G8_SA(b, h) + aoff + m * 2048 + k * 1024); } while (0)
; #define G8_LDB(dst, b, h) do { _Pragma("unroll") for (int n = 0; n < 2; ++n) _Pragma("unroll") for (int k = 0; k < 2; ++k) dst[n][k] = *(const LAS bf16x8*)(lds + G8_SB(b, h) + boff + n * 2048 + k * 1024); } while (0)
; #define G8_WAIT_V(n) asm volatile("s_waitcnt vmcnt(" #n ")" ::: "memory")
; #define G8_WAIT_L(n) asm volatile("s_waitcnt lgkmcnt(" #n ")" ::: "memory")
; #define G8_BAR __builtin_amdgcn_s_barrier()
; #define G8_SCHED __builtin_amdgcn_sched_barrier(0)
;     ...
;             G8_WAIT_L(0); if (do0) G8_MMA(0, 1, At, B1); G8_BAR;
;             G8_LDA(At, 0, 1); G8_STAGE(G8_SA(0, 0), a2, o00, o01);
;             G8_BAR; G8_WAIT_L(0); if (do1) G8_MMA(1, 0, At, B0); G8_BAR; G8_SCHED;
;             G8_STAGE(G8_SB(0, 1), b2 + hstepB, voffB[0], voffB[1]);
;             if constexpr (CONV) G8_WAIT_V(9); else G8_WAIT_V(6);
;             G8_BAR; if (do1) G8_MMA(1, 1, At, B1); G8_BAR;
;             G8_LDB(B0, 1, 0); G8_SCHED; G8_LDA(At, 1, 0); G8_STAGE(G8_SA(0, 1), a2, o10, o11);
;             G8_WAIT_L(8); G8_BAR; G8_WAIT_L(0); if (do0) G8_MMA(0, 0, At, B0); G8_BAR; G8_SCHED;
.LBB0_241:
	s_add_u32 s40, s42, 0x8000
	s_addc_u32 s41, s43, 0
	s_and_b32 s49, s62, 3
	s_lshl_b32 s4, s49, 7
	s_add_u32 s4, s28, s4
	v_lshrrev_b32_e32 v212, 3, v194
	v_lshlrev_b32_e32 v194, 4, v194
	s_addc_u32 s5, s29, 0
	s_mul_i32 s64, s14, s8
	v_and_b32_e32 v194, 0x70, v194
	s_mul_hi_u32 s62, s14, s8
	s_add_u32 s4, s4, s64
	v_mad_u64_u32 v[212:213], vcc, s14, v212, v[194:195]
	s_addc_u32 s5, s5, s62
	s_add_i32 m0, s50, 0x20000
	s_lshl_b64 vcc, s[14:15], 6
	global_load_lds_dwordx4 v212, s[4:5] nt
	s_add_u32 s4, s4, vcc_lo
	s_addc_u32 s5, s5, vcc_hi
	s_mov_b32 m0, s24
	s_lshl_b32 s49, s49, 12
	global_load_lds_dwordx4 v212, s[4:5] nt
	s_waitcnt lgkmcnt(0)
	s_nop 0
	s_waitcnt lgkmcnt(0)
	v_mfma_f32_16x16x32_bf16 v[94:97], v[146:149], v[186:189], v[94:97]
	v_mfma_f32_16x16x32_bf16 v[90:93], v[154:157], v[186:189], v[90:93]
	v_mfma_f32_16x16x32_bf16 v[86:89], v[146:149], v[178:181], v[86:89]
	v_mfma_f32_16x16x32_bf16 v[82:85], v[154:157], v[178:181], v[82:85]
	v_mfma_f32_16x16x32_bf16 v[78:81], v[146:149], v[170:173], v[78:81]
	v_mfma_f32_16x16x32_bf16 v[74:77], v[154:157], v[170:173], v[74:77]
	v_mfma_f32_16x16x32_bf16 v[70:73], v[146:149], v[162:165], v[70:73]
	v_mfma_f32_16x16x32_bf16 v[66:69], v[154:157], v[162:165], v[66:69]
	v_mfma_f32_16x16x32_bf16 v[94:97], v[150:153], v[190:193], v[94:97]
	v_mfma_f32_16x16x32_bf16 v[90:93], v[158:161], v[190:193], v[90:93]
	v_mfma_f32_16x16x32_bf16 v[86:89], v[150:153], v[182:185], v[86:89]
	v_mfma_f32_16x16x32_bf16 v[82:85], v[158:161], v[182:185], v[82:85]
	v_mfma_f32_16x16x32_bf16 v[78:81], v[150:153], v[174:177], v[78:81]
	v_mfma_f32_16x16x32_bf16 v[74:77], v[158:161], v[174:177], v[74:77]
	v_mfma_f32_16x16x32_bf16 v[70:73], v[150:153], v[166:169], v[70:73]
	v_mfma_f32_16x16x32_bf16 v[66:69], v[158:161], v[166:169], v[66:69]
	s_nop 0
	v_mov_b32_e32 v194, v202
	v_mov_b32_e32 v212, v201
	s_mov_b32 m0, s78
	s_barrier
	ds_read_b128 v[162:165], v210 offset:16384
	ds_read_b128 v[166:169], v210 offset:17408
	ds_read_b128 v[170:173], v210 offset:18432
	ds_read_b128 v[174:177], v210 offset:19456
	ds_read_b128 v[178:181], v210 offset:20480
	ds_read_b128 v[182:185], v210 offset:21504
	ds_read_b128 v[186:189], v210 offset:22528
	ds_read_b128 v[190:193], v210 offset:23552
	s_nop 0
	global_load_lds_dwordx4 v212, s[46:47]
	s_mov_b32 m0, s79
	s_nop 0
	global_load_lds_dwordx4 v194, s[46:47]
	s_barrier
	s_waitcnt lgkmcnt(0)
	s_nop 0
	s_waitcnt lgkmcnt(0)
	v_mfma_f32_16x16x32_bf16 v[62:65], v[130:133], v[162:165], v[62:65]
	v_mfma_f32_16x16x32_bf16 v[58:61], v[138:141], v[162:165], v[58:61]
	v_mfma_f32_16x16x32_bf16 v[54:57], v[130:133], v[170:173], v[54:57]
	v_mfma_f32_16x16x32_bf16 v[50:53], v[138:141], v[170:173], v[50:53]
	v_mfma_f32_16x16x32_bf16 v[38:41], v[130:133], v[178:181], v[38:41]
	v_mfma_f32_16x16x32_bf16 v[34:37], v[138:141], v[178:181], v[34:37]
	v_mfma_f32_16x16x32_bf16 v[22:25], v[130:133], v[186:189], v[22:25]
	v_mfma_f32_16x16x32_bf16 v[18:21], v[138:141], v[186:189], v[18:21]
	v_mfma_f32_16x16x32_bf16 v[62:65], v[134:137], v[166:169], v[62:65]
	v_mfma_f32_16x16x32_bf16 v[58:61], v[142:145], v[166:169], v[58:61]
	v_mfma_f32_16x16x32_bf16 v[54:57], v[134:137], v[174:177], v[54:57]
	v_mfma_f32_16x16x32_bf16 v[50:53], v[142:145], v[174:177], v[50:53]
	v_mfma_f32_16x16x32_bf16 v[38:41], v[134:137], v[182:185], v[38:41]
	v_mfma_f32_16x16x32_bf16 v[34:37], v[142:145], v[182:185], v[34:37]
	v_mfma_f32_16x16x32_bf16 v[22:25], v[134:137], v[190:193], v[22:25]
	v_mfma_f32_16x16x32_bf16 v[18:21], v[142:145], v[190:193], v[18:21]
	s_nop 0
	s_barrier
	s_add_u32 s4, s42, 0x4000
	v_mov_b32_e32 v130, v1
	v_mov_b32_e32 v131, v198
	s_addc_u32 s5, s43, 0
	s_mov_b32 m0, s80
	s_nop 0
	global_load_lds_dwordx4 v130, s[4:5]
	s_mov_b32 m0, s81
	s_nop 0
	global_load_lds_dwordx4 v131, s[4:5]
	s_waitcnt vmcnt(9)
	s_barrier
	s_nop 0
	v_mfma_f32_16x16x32_bf16 v[46:49], v[146:149], v[162:165], v[46:49]
	v_mfma_f32_16x16x32_bf16 v[42:45], v[154:157], v[162:165], v[42:45]
	v_mfma_f32_16x16x32_bf16 v[30:33], v[146:149], v[170:173], v[30:33]
	v_mfma_f32_16x16x32_bf16 v[26:29], v[154:157], v[170:173], v[26:29]
	v_mfma_f32_16x16x32_bf16 v[14:17], v[146:149], v[178:181], v[14:17]
	v_mfma_f32_16x16x32_bf16 v[10:13], v[154:157], v[178:181], v[10:13]
	v_mfma_f32_16x16x32_bf16 v[6:9], v[146:149], v[186:189], v[6:9]
	v_mfma_f32_16x16x32_bf16 v[2:5], v[154:157], v[186:189], v[2:5]
	v_mfma_f32_16x16x32_bf16 v[46:49], v[150:153], v[166:169], v[46:49]
	v_mfma_f32_16x16x32_bf16 v[42:45], v[158:161], v[166:169], v[42:45]
	v_mfma_f32_16x16x32_bf16 v[30:33], v[150:153], v[174:177], v[30:33]
	v_mfma_f32_16x16x32_bf16 v[26:29], v[158:161], v[174:177], v[26:29]
	v_mfma_f32_16x16x32_bf16 v[14:17], v[150:153], v[182:185], v[14:17]
	v_mfma_f32_16x16x32_bf16 v[10:13], v[158:161], v[182:185], v[10:13]
	v_mfma_f32_16x16x32_bf16 v[6:9], v[150:153], v[190:193], v[6:9]
	v_mfma_f32_16x16x32_bf16 v[2:5], v[158:161], v[190:193], v[2:5]
	s_nop 0
	s_add_i32 s4, 0, 0x18000
	v_add_u32_e32 v142, s4, v209
	s_barrier
	ds_read_b128 v[130:133], v142
	ds_read_b128 v[134:137], v142 offset:1024
	ds_read_b128 v[138:141], v142 offset:2048
	ds_read_b128 v[142:145], v142 offset:3072
	v_mov_b32_e32 v178, v203
	v_mov_b32_e32 v179, v204
	s_mov_b32 m0, s82
	ds_read_b128 v[146:149], v210 offset:32768
	ds_read_b128 v[150:153], v210 offset:33792
	ds_read_b128 v[154:157], v210 offset:34816
	ds_read_b128 v[158:161], v210 offset:35840
	ds_read_b128 v[162:165], v210 offset:36864
	ds_read_b128 v[166:169], v210 offset:37888
	ds_read_b128 v[170:173], v210 offset:38912
	ds_read_b128 v[174:177], v210 offset:39936
	s_nop 0
	global_load_lds_dwordx4 v178, s[46:47]
	s_mov_b32 m0, s83
	s_nop 0
	global_load_lds_dwordx4 v179, s[46:47]
	s_waitcnt lgkmcnt(8)
	s_barrier
; #define G8_STAGE(bufoff, gbase, v0, v1) do { unsigned x0_ = (v0), x1_ = (v1); asm volatile("" : "+v"(x0_), "+v"(x1_));     \
;         __builtin_amdgcn_global_load_lds((const unsigned*)((gbase) + x0_), (LAS unsigned*)(lds + (bufoff) + ldsw), 16, 0, 0); \
;         __builtin_amdgcn_global_load_lds((const unsigned*)((gbase) + x1_), (LAS unsigned*)(lds + (bufoff) + ldsw + 8192), 16, 0, 0); } while (0)
; #define G8_LDA(dst, b, h) do { _Pragma("unroll") for (int m = 0; m < 4; ++m) _Pragma("unroll") for (int k = 0; k < 2; ++k) dst[m][k] = *(const LAS bf16x8*)(lds + G8_SA(b, h) + aoff + m * 2048 + k * 1024); } while (0)
; #define G8_LDB(dst, b, h) do { _Pragma("unroll") for (int n = 0; n < 2; ++n) _Pragma("unroll") for (int k = 0; k < 2; ++k) dst[n][k] = *(const LAS bf16x8*)(lds + G8_SB(b, h) + boff + n * 2048 + k * 1024); } while (0)
; #define G8_WAIT_V(n) asm volatile("s_waitcnt vmcnt(" #n ")" ::: "memory")
; #define G8_WAIT_L(n) asm volatile("s_waitcnt lgkmcnt(" #n ")" ::: "memory")
; #define G8_BAR __builtin_amdgcn_s_barrier()
; #define G8_SCHED __builtin_amdgcn_sched_barrier(0)
;     ...
;             G8_WAIT_L(8); G8_BAR; G8_WAIT_L(0); if (do0) G8_MMA(0, 0, At, B0); G8_BAR; G8_SCHED;
;             G8_LDB(B1, 1, 1); G8_STAGE(G8_SB(1, 0), b3, voffB[0], voffB[1]);
;             G8_BAR; G8_WAIT_L(0); if (do0) G8_MMA(0, 1, At, B1); G8_BAR;
;             G8_LDA(At, 1, 1); G8_STAGE(G8_SA(1, 0), a3, o00, o01);
;             G8_BAR; G8_WAIT_L(0); if (do1) G8_MMA(1, 0, At, B0); G8_BAR; G8_SCHED;
;             G8_STAGE(G8_SB(1, 1), b3 + hstepB, voffB[0], voffB[1]);
;             G8_WAIT_V(6); G8_BAR; if (do1) G8_MMA(1, 1, At, B1); G8_BAR;
;         }
	s_waitcnt lgkmcnt(0)
	s_nop 0
	s_waitcnt lgkmcnt(0)
	v_mfma_f32_16x16x32_bf16 v[126:129], v[130:133], v[146:149], v[126:129]
	v_mfma_f32_16x16x32_bf16 v[122:125], v[138:141], v[146:149], v[122:125]
	v_mfma_f32_16x16x32_bf16 v[118:121], v[130:133], v[154:157], v[118:121]
	v_mfma_f32_16x16x32_bf16 v[114:117], v[138:141], v[154:157], v[114:117]
	v_mfma_f32_16x16x32_bf16 v[110:113], v[130:133], v[162:165], v[110:113]
	v_mfma_f32_16x16x32_bf16 v[106:109], v[138:141], v[162:165], v[106:109]
	v_mfma_f32_16x16x32_bf16 v[102:105], v[130:133], v[170:173], v[102:105]
	v_mfma_f32_16x16x32_bf16 v[98:101], v[138:141], v[170:173], v[98:101]
	v_mfma_f32_16x16x32_bf16 v[126:129], v[134:137], v[150:153], v[126:129]
	v_mfma_f32_16x16x32_bf16 v[122:125], v[142:145], v[150:153], v[122:125]
	v_mfma_f32_16x16x32_bf16 v[118:121], v[134:137], v[158:161], v[118:121]
	v_mfma_f32_16x16x32_bf16 v[114:117], v[142:145], v[158:161], v[114:117]
	v_mfma_f32_16x16x32_bf16 v[110:113], v[134:137], v[166:169], v[110:113]
	v_mfma_f32_16x16x32_bf16 v[106:109], v[142:145], v[166:169], v[106:109]
	v_mfma_f32_16x16x32_bf16 v[102:105], v[134:137], v[174:177], v[102:105]
	v_mfma_f32_16x16x32_bf16 v[98:101], v[142:145], v[174:177], v[98:101]
	s_nop 0
	s_barrier
	s_add_i32 s62, 0, 0x1c000
	s_add_i32 s4, s4, s77
	v_add_u32_e32 v190, s62, v209
	v_mov_b32_e32 v194, v1
	v_mov_b32_e32 v212, v198
	s_mov_b32 m0, s4
	ds_read_b128 v[178:181], v190
	ds_read_b128 v[182:185], v190 offset:1024
	ds_read_b128 v[186:189], v190 offset:2048
	ds_read_b128 v[190:193], v190 offset:3072
	s_nop 0
	global_load_lds_dwordx4 v194, s[40:41]
	s_add_i32 m0, s4, 0x2000
	s_nop 0
	global_load_lds_dwordx4 v212, s[40:41]
	s_barrier
	s_waitcnt lgkmcnt(0)
	s_nop 0
	s_waitcnt lgkmcnt(0)
	v_mfma_f32_16x16x32_bf16 v[94:97], v[178:181], v[146:149], v[94:97]
	v_mfma_f32_16x16x32_bf16 v[90:93], v[186:189], v[146:149], v[90:93]
	v_mfma_f32_16x16x32_bf16 v[86:89], v[178:181], v[154:157], v[86:89]
	v_mfma_f32_16x16x32_bf16 v[82:85], v[186:189], v[154:157], v[82:85]
	v_mfma_f32_16x16x32_bf16 v[78:81], v[178:181], v[162:165], v[78:81]
	v_mfma_f32_16x16x32_bf16 v[74:77], v[186:189], v[162:165], v[74:77]
	v_mfma_f32_16x16x32_bf16 v[70:73], v[178:181], v[170:173], v[70:73]
	v_mfma_f32_16x16x32_bf16 v[66:69], v[186:189], v[170:173], v[66:69]
	v_mfma_f32_16x16x32_bf16 v[94:97], v[182:185], v[150:153], v[94:97]
	v_mfma_f32_16x16x32_bf16 v[90:93], v[190:193], v[150:153], v[90:93]
	v_mfma_f32_16x16x32_bf16 v[86:89], v[182:185], v[158:161], v[86:89]
	v_mfma_f32_16x16x32_bf16 v[82:85], v[190:193], v[158:161], v[82:85]
	v_mfma_f32_16x16x32_bf16 v[78:81], v[182:185], v[166:169], v[78:81]
	v_mfma_f32_16x16x32_bf16 v[74:77], v[190:193], v[166:169], v[74:77]
	v_mfma_f32_16x16x32_bf16 v[70:73], v[182:185], v[174:177], v[70:73]
	v_mfma_f32_16x16x32_bf16 v[66:69], v[190:193], v[174:177], v[66:69]
	s_nop 0
	v_mov_b32_e32 v212, v202
	v_mov_b32_e32 v194, v201
	s_barrier
	ds_read_b128 v[146:149], v210 offset:49152
	ds_read_b128 v[150:153], v210 offset:50176
	ds_read_b128 v[154:157], v210 offset:51200
	ds_read_b128 v[158:161], v210 offset:52224
	ds_read_b128 v[162:165], v210 offset:53248
	ds_read_b128 v[166:169], v210 offset:54272
	ds_read_b128 v[170:173], v210 offset:55296
	ds_read_b128 v[174:177], v210 offset:56320
	v_mov_b32_e32 v213, v195
	v_lshl_add_u64 v[214:215], s[46:47], 0, v[194:195]
	s_mov_b32 m0, s90
	v_lshl_add_u64 v[214:215], v[214:215], 0, s[26:27]
	v_lshl_add_u64 v[212:213], s[46:47], 0, v[212:213]
	global_load_lds_dwordx4 v[214:215], off
	v_lshl_add_u64 v[212:213], v[212:213], 0, s[26:27]
	s_mov_b32 m0, s91
	s_nop 0
	global_load_lds_dwordx4 v[212:213], off
	s_barrier
	s_waitcnt lgkmcnt(0)
	s_nop 0
	s_waitcnt lgkmcnt(0)
	v_mfma_f32_16x16x32_bf16 v[62:65], v[130:133], v[146:149], v[62:65]
	v_mfma_f32_16x16x32_bf16 v[58:61], v[138:141], v[146:149], v[58:61]
	v_mfma_f32_16x16x32_bf16 v[54:57], v[130:133], v[154:157], v[54:57]
	v_mfma_f32_16x16x32_bf16 v[50:53], v[138:141], v[154:157], v[50:53]
	v_mfma_f32_16x16x32_bf16 v[38:41], v[130:133], v[162:165], v[38:41]
	v_mfma_f32_16x16x32_bf16 v[34:37], v[138:141], v[162:165], v[34:37]
	v_mfma_f32_16x16x32_bf16 v[22:25], v[130:133], v[170:173], v[22:25]
	v_mfma_f32_16x16x32_bf16 v[18:21], v[138:141], v[170:173], v[18:21]
	v_mfma_f32_16x16x32_bf16 v[62:65], v[134:137], v[150:153], v[62:65]
	v_mfma_f32_16x16x32_bf16 v[58:61], v[142:145], v[150:153], v[58:61]
	v_mfma_f32_16x16x32_bf16 v[54:57], v[134:137], v[158:161], v[54:57]
	v_mfma_f32_16x16x32_bf16 v[50:53], v[142:145], v[158:161], v[50:53]
	v_mfma_f32_16x16x32_bf16 v[38:41], v[134:137], v[166:169], v[38:41]
	v_mfma_f32_16x16x32_bf16 v[34:37], v[142:145], v[166:169], v[34:37]
	v_mfma_f32_16x16x32_bf16 v[22:25], v[134:137], v[174:177], v[22:25]
	v_mfma_f32_16x16x32_bf16 v[18:21], v[142:145], v[174:177], v[18:21]
	s_nop 0
	s_barrier
	s_add_u32 s4, s42, 0xc000
	s_addc_u32 s5, s43, 0
	s_add_i32 s40, s62, s77
	v_mov_b32_e32 v130, v1
	v_mov_b32_e32 v131, v198
	s_mov_b32 m0, s40
	s_nop 0
	global_load_lds_dwordx4 v130, s[4:5]
	s_add_i32 m0, s40, 0x2000
	s_nop 0
	global_load_lds_dwordx4 v131, s[4:5]
	s_waitcnt vmcnt(6)
	s_barrier
	s_nop 0
	v_mfma_f32_16x16x32_bf16 v[46:49], v[178:181], v[146:149], v[46:49]
	s_add_u32 s40, s30, s49
	s_addc_u32 s41, s31, 0
	v_mfma_f32_16x16x32_bf16 v[42:45], v[186:189], v[146:149], v[42:45]
	v_mfma_f32_16x16x32_bf16 v[30:33], v[178:181], v[154:157], v[30:33]
	v_mfma_f32_16x16x32_bf16 v[26:29], v[186:189], v[154:157], v[26:29]
	v_mfma_f32_16x16x32_bf16 v[14:17], v[178:181], v[162:165], v[14:17]
	v_mfma_f32_16x16x32_bf16 v[10:13], v[186:189], v[162:165], v[10:13]
	v_mfma_f32_16x16x32_bf16 v[6:9], v[178:181], v[170:173], v[6:9]
	v_mfma_f32_16x16x32_bf16 v[2:5], v[186:189], v[170:173], v[2:5]
	v_mfma_f32_16x16x32_bf16 v[46:49], v[182:185], v[150:153], v[46:49]
	v_mfma_f32_16x16x32_bf16 v[42:45], v[190:193], v[150:153], v[42:45]
	v_mfma_f32_16x16x32_bf16 v[30:33], v[182:185], v[158:161], v[30:33]
	v_mfma_f32_16x16x32_bf16 v[26:29], v[190:193], v[158:161], v[26:29]
	v_mfma_f32_16x16x32_bf16 v[14:17], v[182:185], v[166:169], v[14:17]
	v_mfma_f32_16x16x32_bf16 v[10:13], v[190:193], v[166:169], v[10:13]
	v_mfma_f32_16x16x32_bf16 v[6:9], v[182:185], v[174:177], v[6:9]
	v_mfma_f32_16x16x32_bf16 v[2:5], v[190:193], v[174:177], v[2:5]
	s_nop 0
	s_add_i32 s61, s61, 2
	s_add_u32 s6, s6, 0x10000
	s_addc_u32 s7, s7, 0
	s_add_u32 s0, s0, 0x100
	s_addc_u32 s1, s1, 0
	s_add_i32 s49, s68, 1
	s_cmp_gt_u32 s61, 29
	s_barrier
	s_cbranch_scc1 .LBB0_243
	s_mov_b32 s68, s49
	s_branch .LBB0_234

; #define G8_STAGE(bufoff, gbase, v0, v1) do { unsigned x0_ = (v0), x1_ = (v1); asm volatile("" : "+v"(x0_), "+v"(x1_));     \
;         __builtin_amdgcn_global_load_lds((const unsigned*)((gbase) + x0_), (LAS unsigned*)(lds + (bufoff) + ldsw), 16, 0, 0); \
;         __builtin_amdgcn_global_load_lds((const unsigned*)((gbase) + x1_), (LAS unsigned*)(lds + (bufoff) + ldsw + 8192), 16, 0, 0); } while (0)
; #define G8_LDA(dst, b, h) do { _Pragma("unroll") for (int m = 0; m < 4; ++m) _Pragma("unroll") for (int k = 0; k < 2; ++k) dst[m][k] = *(const LAS bf16x8*)(lds + G8_SA(b, h) + aoff + m * 2048 + k * 1024); } while (0)
; #define G8_LDB(dst, b, h) do { _Pragma("unroll") for (int n = 0; n < 2; ++n) _Pragma("unroll") for (int k = 0; k < 2; ++k) dst[n][k] = *(const LAS bf16x8*)(lds + G8_SB(b, h) + boff + n * 2048 + k * 1024); } while (0)
; #define G8_WAIT_L(n) asm volatile("s_waitcnt lgkmcnt(" #n ")" ::: "memory")
; #define G8_BAR __builtin_amdgcn_s_barrier()
; #define G8_SCHED __builtin_amdgcn_sched_barrier(0)
;     ...
;             G8_CONV_READ; G8_SCHED;
;             G8_LDB(B0, 0, 0); G8_SCHED; G8_LDA(At, 0, 0); G8_STAGE(G8_SA(1, 1), a1, cv[1][0], cv[1][1]);
;             G8_WAIT_L(8); G8_BAR; G8_WAIT_L(0); if (do0) G8_MMA(0, 0, At, B0); G8_CONV_CVT; G8_BAR; G8_SCHED;
;             G8_LDB(B1, 0, 1); G8_STAGE(G8_SB(0, 0), b2, voffB[0], voffB[1]);
;             G8_BAR; G8_CONV_ISSUE;
;             G8_WAIT_L(0); if (do0) G8_MMA(0, 1, At, B1); G8_BAR;
;             G8_LDA(At, 0, 1); G8_STAGE(G8_SA(0, 0), a2, o00, o01);
;             G8_BAR; G8_WAIT_L(0); if (do1) G8_MMA(1, 0, At, B0); G8_BAR; G8_SCHED;
.LBB0_536:
	s_add_u32 s66, s28, 0x80
	s_addc_u32 s67, s29, 0
	s_add_u32 s28, s28, 0x100
	s_addc_u32 s29, s29, 0
	s_add_u32 s30, s30, 0x10000
	s_addc_u32 s31, s31, 0
	s_cmp_eq_u32 s64, 12
	s_cselect_b32 s37, s0, s29
	s_cselect_b32 s36, s61, s28
	s_cselect_b32 s35, s62, s31
	s_cselect_b32 s34, s63, s30
	ds_read_b128 v[130:133], v175
	ds_read_b128 v[134:137], v175 offset:1024
	ds_read_b128 v[138:141], v175 offset:2048
	ds_read_b128 v[142:145], v175 offset:3072
	s_add_u32 s38, s34, 0x8000
	s_addc_u32 s39, s35, 0
	v_mov_b32_e32 v146, v176
	v_mov_b32_e32 v192, v174
	s_add_i32 m0, s41, 0xc000
	ds_read_b128 v[150:153], v177
	ds_read_b128 v[154:157], v177 offset:1024
	ds_read_b128 v[158:161], v177 offset:2048
	ds_read_b128 v[162:165], v177 offset:3072
	ds_read_b128 v[166:169], v177 offset:4096
	ds_read_b128 v[180:183], v177 offset:5120
	ds_read_b128 v[184:187], v177 offset:6144
	ds_read_b128 v[188:191], v177 offset:7168
	s_nop 0
	global_load_lds_dwordx4 v192, s[66:67]
	s_add_i32 m0, s41, 0xe000
	s_nop 0
	global_load_lds_dwordx4 v146, s[66:67]
	s_waitcnt lgkmcnt(8)
	s_barrier
	s_waitcnt lgkmcnt(0)
	s_nop 0
	s_waitcnt lgkmcnt(0)
	v_mfma_f32_16x16x32_bf16 v[126:129], v[130:133], v[150:153], v[126:129]
	v_mfma_f32_16x16x32_bf16 v[122:125], v[138:141], v[150:153], v[122:125]
	v_mfma_f32_16x16x32_bf16 v[110:113], v[130:133], v[158:161], v[110:113]
	v_mfma_f32_16x16x32_bf16 v[106:109], v[138:141], v[158:161], v[106:109]
	v_mfma_f32_16x16x32_bf16 v[94:97], v[130:133], v[166:169], v[94:97]
	v_mfma_f32_16x16x32_bf16 v[90:93], v[138:141], v[166:169], v[90:93]
	v_mfma_f32_16x16x32_bf16 v[78:81], v[130:133], v[184:187], v[78:81]
	v_mfma_f32_16x16x32_bf16 v[74:77], v[138:141], v[184:187], v[74:77]
	v_mfma_f32_16x16x32_bf16 v[126:129], v[134:137], v[154:157], v[126:129]
	v_mfma_f32_16x16x32_bf16 v[122:125], v[142:145], v[154:157], v[122:125]
	v_mfma_f32_16x16x32_bf16 v[110:113], v[134:137], v[162:165], v[110:113]
	v_mfma_f32_16x16x32_bf16 v[106:109], v[142:145], v[162:165], v[106:109]
	v_mfma_f32_16x16x32_bf16 v[94:97], v[134:137], v[180:183], v[94:97]
	v_mfma_f32_16x16x32_bf16 v[90:93], v[142:145], v[180:183], v[90:93]
	v_mfma_f32_16x16x32_bf16 v[78:81], v[134:137], v[188:191], v[78:81]
	v_mfma_f32_16x16x32_bf16 v[74:77], v[142:145], v[188:191], v[74:77]
	s_nop 0
	s_barrier
	s_add_i32 s65, s52, s40
	v_mov_b32_e32 v146, v171
	v_mov_b32_e32 v208, v170
	s_mov_b32 m0, s65
	ds_read_b128 v[192:195], v178
	ds_read_b128 v[196:199], v178 offset:1024
	ds_read_b128 v[200:203], v178 offset:2048
	ds_read_b128 v[204:207], v178 offset:3072
	s_nop 0
	global_load_lds_dwordx4 v208, s[34:35]
	s_add_i32 m0, s65, 0x2000
	s_nop 0
	global_load_lds_dwordx4 v146, s[34:35]
	s_barrier
	s_waitcnt lgkmcnt(0)
	s_nop 0
	s_waitcnt lgkmcnt(0)
	v_mfma_f32_16x16x32_bf16 v[118:121], v[192:195], v[150:153], v[118:121]
	v_mfma_f32_16x16x32_bf16 v[114:117], v[200:203], v[150:153], v[114:117]
	v_mfma_f32_16x16x32_bf16 v[102:105], v[192:195], v[158:161], v[102:105]
	v_mfma_f32_16x16x32_bf16 v[98:101], v[200:203], v[158:161], v[98:101]
	v_mfma_f32_16x16x32_bf16 v[86:89], v[192:195], v[166:169], v[86:89]
	v_mfma_f32_16x16x32_bf16 v[82:85], v[200:203], v[166:169], v[82:85]
	v_mfma_f32_16x16x32_bf16 v[70:73], v[192:195], v[184:187], v[70:73]
	v_mfma_f32_16x16x32_bf16 v[66:69], v[200:203], v[184:187], v[66:69]
	v_mfma_f32_16x16x32_bf16 v[118:121], v[196:199], v[154:157], v[118:121]
	v_mfma_f32_16x16x32_bf16 v[114:117], v[204:207], v[154:157], v[114:117]
	v_mfma_f32_16x16x32_bf16 v[102:105], v[196:199], v[162:165], v[102:105]
	v_mfma_f32_16x16x32_bf16 v[98:101], v[204:207], v[162:165], v[98:101]
	v_mfma_f32_16x16x32_bf16 v[86:89], v[196:199], v[180:183], v[86:89]
	v_mfma_f32_16x16x32_bf16 v[82:85], v[204:207], v[180:183], v[82:85]
	v_mfma_f32_16x16x32_bf16 v[70:73], v[196:199], v[188:191], v[70:73]
	v_mfma_f32_16x16x32_bf16 v[66:69], v[204:207], v[188:191], v[66:69]
	s_nop 0
	v_mov_b32_e32 v146, v173
	v_mov_b32_e32 v208, v172
	s_mov_b32 m0, s41
	s_barrier
	ds_read_b128 v[150:153], v177 offset:16384
	ds_read_b128 v[154:157], v177 offset:17408
	ds_read_b128 v[158:161], v177 offset:18432
	ds_read_b128 v[162:165], v177 offset:19456
	ds_read_b128 v[166:169], v177 offset:20480
	ds_read_b128 v[180:183], v177 offset:21504
	ds_read_b128 v[184:187], v177 offset:22528
	ds_read_b128 v[188:191], v177 offset:23552
	s_nop 0
	global_load_lds_dwordx4 v208, s[36:37]
	s_mov_b32 m0, s42
	s_nop 0
	global_load_lds_dwordx4 v146, s[36:37]
	s_barrier
	s_waitcnt lgkmcnt(0)
	s_nop 0
	s_waitcnt lgkmcnt(0)
	v_mfma_f32_16x16x32_bf16 v[62:65], v[130:133], v[150:153], v[62:65]
	v_mfma_f32_16x16x32_bf16 v[58:61], v[138:141], v[150:153], v[58:61]
	v_mfma_f32_16x16x32_bf16 v[46:49], v[130:133], v[158:161], v[46:49]
	v_mfma_f32_16x16x32_bf16 v[42:45], v[138:141], v[158:161], v[42:45]
	v_mfma_f32_16x16x32_bf16 v[30:33], v[130:133], v[166:169], v[30:33]
	v_mfma_f32_16x16x32_bf16 v[26:29], v[138:141], v[166:169], v[26:29]
	v_mfma_f32_16x16x32_bf16 v[14:17], v[130:133], v[184:187], v[14:17]
	v_mfma_f32_16x16x32_bf16 v[10:13], v[138:141], v[184:187], v[10:13]
	v_mfma_f32_16x16x32_bf16 v[62:65], v[134:137], v[154:157], v[62:65]
	v_mfma_f32_16x16x32_bf16 v[58:61], v[142:145], v[154:157], v[58:61]
	v_mfma_f32_16x16x32_bf16 v[46:49], v[134:137], v[162:165], v[46:49]
	v_mfma_f32_16x16x32_bf16 v[42:45], v[142:145], v[162:165], v[42:45]
	v_mfma_f32_16x16x32_bf16 v[30:33], v[134:137], v[180:183], v[30:33]
	v_mfma_f32_16x16x32_bf16 v[26:29], v[142:145], v[180:183], v[26:29]
	v_mfma_f32_16x16x32_bf16 v[14:17], v[134:137], v[188:191], v[14:17]
	v_mfma_f32_16x16x32_bf16 v[10:13], v[142:145], v[188:191], v[10:13]
	s_nop 0
	s_barrier
; #define G8_STAGE(bufoff, gbase, v0, v1) do { unsigned x0_ = (v0), x1_ = (v1); asm volatile("" : "+v"(x0_), "+v"(x1_));     \
;         __builtin_amdgcn_global_load_lds((const unsigned*)((gbase) + x0_), (LAS unsigned*)(lds + (bufoff) + ldsw), 16, 0, 0); \
;         __builtin_amdgcn_global_load_lds((const unsigned*)((gbase) + x1_), (LAS unsigned*)(lds + (bufoff) + ldsw + 8192), 16, 0, 0); } while (0)
; #define G8_LDA(dst, b, h) do { _Pragma("unroll") for (int m = 0; m < 4; ++m) _Pragma("unroll") for (int k = 0; k < 2; ++k) dst[m][k] = *(const LAS bf16x8*)(lds + G8_SA(b, h) + aoff + m * 2048 + k * 1024); } while (0)
; #define G8_LDB(dst, b, h) do { _Pragma("unroll") for (int n = 0; n < 2; ++n) _Pragma("unroll") for (int k = 0; k < 2; ++k) dst[n][k] = *(const LAS bf16x8*)(lds + G8_SB(b, h) + boff + n * 2048 + k * 1024); } while (0)
; #define G8_WAIT_V(n) asm volatile("s_waitcnt vmcnt(" #n ")" ::: "memory")
; #define G8_WAIT_L(n) asm volatile("s_waitcnt lgkmcnt(" #n ")" ::: "memory")
; #define G8_BAR __builtin_amdgcn_s_barrier()
; #define G8_SCHED __builtin_amdgcn_sched_barrier(0)
;     ...
;             G8_STAGE(G8_SB(0, 1), b2 + hstepB, voffB[0], voffB[1]);
;             if constexpr (CONV) G8_WAIT_V(9); else G8_WAIT_V(6);
;             G8_BAR; if (do1) G8_MMA(1, 1, At, B1); G8_BAR;
;             G8_LDB(B0, 1, 0); G8_SCHED; G8_LDA(At, 1, 0); G8_STAGE(G8_SA(0, 1), a2, o10, o11);
;             G8_WAIT_L(8); G8_BAR; G8_WAIT_L(0); if (do0) G8_MMA(0, 0, At, B0); G8_BAR; G8_SCHED;
;             G8_LDB(B1, 1, 1); G8_STAGE(G8_SB(1, 0), b3, voffB[0], voffB[1]);
;             G8_BAR; G8_WAIT_L(0); if (do0) G8_MMA(0, 1, At, B1); G8_BAR;
;             G8_LDA(At, 1, 1); G8_STAGE(G8_SA(1, 0), a3, o00, o01);
	s_add_u32 s66, s34, 0x4000
	s_addc_u32 s67, s35, 0
	s_add_i32 s65, s53, s40
	v_mov_b32_e32 v130, v171
	v_mov_b32_e32 v131, v170
	s_mov_b32 m0, s65
	s_nop 0
	global_load_lds_dwordx4 v131, s[66:67]
	s_add_i32 m0, s65, 0x2000
	s_nop 0
	global_load_lds_dwordx4 v130, s[66:67]
	s_waitcnt vmcnt(6)
	s_barrier
	s_nop 0
	v_mfma_f32_16x16x32_bf16 v[54:57], v[192:195], v[150:153], v[54:57]
	v_mfma_f32_16x16x32_bf16 v[50:53], v[200:203], v[150:153], v[50:53]
	v_mfma_f32_16x16x32_bf16 v[38:41], v[192:195], v[158:161], v[38:41]
	v_mfma_f32_16x16x32_bf16 v[34:37], v[200:203], v[158:161], v[34:37]
	v_mfma_f32_16x16x32_bf16 v[22:25], v[192:195], v[166:169], v[22:25]
	v_mfma_f32_16x16x32_bf16 v[18:21], v[200:203], v[166:169], v[18:21]
	v_mfma_f32_16x16x32_bf16 v[6:9], v[192:195], v[184:187], v[6:9]
	v_mfma_f32_16x16x32_bf16 v[2:5], v[200:203], v[184:187], v[2:5]
	v_mfma_f32_16x16x32_bf16 v[54:57], v[196:199], v[154:157], v[54:57]
	v_mfma_f32_16x16x32_bf16 v[50:53], v[204:207], v[154:157], v[50:53]
	v_mfma_f32_16x16x32_bf16 v[38:41], v[196:199], v[162:165], v[38:41]
	v_mfma_f32_16x16x32_bf16 v[34:37], v[204:207], v[162:165], v[34:37]
	v_mfma_f32_16x16x32_bf16 v[22:25], v[196:199], v[180:183], v[22:25]
	v_mfma_f32_16x16x32_bf16 v[18:21], v[204:207], v[180:183], v[18:21]
	v_mfma_f32_16x16x32_bf16 v[6:9], v[196:199], v[188:191], v[6:9]
	v_mfma_f32_16x16x32_bf16 v[2:5], v[204:207], v[188:191], v[2:5]
	s_nop 0
	s_add_i32 s65, 0, 0x18000
	v_add_u32_e32 v142, s65, v1
	s_barrier
	ds_read_b128 v[130:133], v142
	ds_read_b128 v[134:137], v142 offset:1024
	ds_read_b128 v[138:141], v142 offset:2048
	ds_read_b128 v[142:145], v142 offset:3072
	v_mov_b32_e32 v146, v176
	v_mov_b32_e32 v192, v174
	s_mov_b32 m0, s43
	ds_read_b128 v[150:153], v177 offset:32768
	ds_read_b128 v[154:157], v177 offset:33792
	ds_read_b128 v[158:161], v177 offset:34816
	ds_read_b128 v[162:165], v177 offset:35840
	ds_read_b128 v[166:169], v177 offset:36864
	ds_read_b128 v[180:183], v177 offset:37888
	ds_read_b128 v[184:187], v177 offset:38912
	ds_read_b128 v[188:191], v177 offset:39936
	s_nop 0
	global_load_lds_dwordx4 v192, s[36:37]
	s_mov_b32 m0, s44
	s_nop 0
	global_load_lds_dwordx4 v146, s[36:37]
	s_waitcnt lgkmcnt(8)
	s_barrier
	s_waitcnt lgkmcnt(0)
	s_nop 0
	s_waitcnt lgkmcnt(0)
	v_mfma_f32_16x16x32_bf16 v[126:129], v[130:133], v[150:153], v[126:129]
	v_mfma_f32_16x16x32_bf16 v[122:125], v[138:141], v[150:153], v[122:125]
	v_mfma_f32_16x16x32_bf16 v[110:113], v[130:133], v[158:161], v[110:113]
	v_mfma_f32_16x16x32_bf16 v[106:109], v[138:141], v[158:161], v[106:109]
	v_mfma_f32_16x16x32_bf16 v[94:97], v[130:133], v[166:169], v[94:97]
	v_mfma_f32_16x16x32_bf16 v[90:93], v[138:141], v[166:169], v[90:93]
	v_mfma_f32_16x16x32_bf16 v[78:81], v[130:133], v[184:187], v[78:81]
	v_mfma_f32_16x16x32_bf16 v[74:77], v[138:141], v[184:187], v[74:77]
	v_mfma_f32_16x16x32_bf16 v[126:129], v[134:137], v[154:157], v[126:129]
	v_mfma_f32_16x16x32_bf16 v[122:125], v[142:145], v[154:157], v[122:125]
	v_mfma_f32_16x16x32_bf16 v[110:113], v[134:137], v[162:165], v[110:113]
	v_mfma_f32_16x16x32_bf16 v[106:109], v[142:145], v[162:165], v[106:109]
	v_mfma_f32_16x16x32_bf16 v[94:97], v[134:137], v[180:183], v[94:97]
	v_mfma_f32_16x16x32_bf16 v[90:93], v[142:145], v[180:183], v[90:93]
	v_mfma_f32_16x16x32_bf16 v[78:81], v[134:137], v[188:191], v[78:81]
	v_mfma_f32_16x16x32_bf16 v[74:77], v[142:145], v[188:191], v[74:77]
	s_nop 0
	s_barrier
	s_add_i32 s66, 0, 0x1c000
	v_add_u32_e32 v146, s66, v1
	s_add_i32 s65, s65, s40
	ds_read_b128 v[192:195], v146
	ds_read_b128 v[196:199], v146 offset:1024
	ds_read_b128 v[200:203], v146 offset:2048
	ds_read_b128 v[204:207], v146 offset:3072
	v_mov_b32_e32 v146, v171
	v_mov_b32_e32 v208, v170
	s_mov_b32 m0, s65
	s_nop 0
	global_load_lds_dwordx4 v208, s[38:39]
	s_add_i32 m0, s65, 0x2000
	s_nop 0
	global_load_lds_dwordx4 v146, s[38:39]
	s_barrier
	s_waitcnt lgkmcnt(0)
	s_nop 0
	s_waitcnt lgkmcnt(0)
	v_mfma_f32_16x16x32_bf16 v[118:121], v[192:195], v[150:153], v[118:121]
	v_mfma_f32_16x16x32_bf16 v[114:117], v[200:203], v[150:153], v[114:117]
	v_mfma_f32_16x16x32_bf16 v[102:105], v[192:195], v[158:161], v[102:105]
	v_mfma_f32_16x16x32_bf16 v[98:101], v[200:203], v[158:161], v[98:101]
	v_mfma_f32_16x16x32_bf16 v[86:89], v[192:195], v[166:169], v[86:89]
	v_mfma_f32_16x16x32_bf16 v[82:85], v[200:203], v[166:169], v[82:85]
	v_mfma_f32_16x16x32_bf16 v[70:73], v[192:195], v[184:187], v[70:73]
	v_mfma_f32_16x16x32_bf16 v[66:69], v[200:203], v[184:187], v[66:69]
	v_mfma_f32_16x16x32_bf16 v[118:121], v[196:199], v[154:157], v[118:121]
	v_mfma_f32_16x16x32_bf16 v[114:117], v[204:207], v[154:157], v[114:117]
	v_mfma_f32_16x16x32_bf16 v[102:105], v[196:199], v[162:165], v[102:105]
	v_mfma_f32_16x16x32_bf16 v[98:101], v[204:207], v[162:165], v[98:101]
	v_mfma_f32_16x16x32_bf16 v[86:89], v[196:199], v[180:183], v[86:89]
	v_mfma_f32_16x16x32_bf16 v[82:85], v[204:207], v[180:183], v[82:85]
	v_mfma_f32_16x16x32_bf16 v[70:73], v[196:199], v[188:191], v[70:73]
	v_mfma_f32_16x16x32_bf16 v[66:69], v[204:207], v[188:191], v[66:69]
	s_nop 0
	v_mov_b32_e32 v208, v173
	v_mov_b32_e32 v146, v172
	s_barrier
	ds_read_b128 v[150:153], v177 offset:49152
	ds_read_b128 v[154:157], v177 offset:50176
	ds_read_b128 v[158:161], v177 offset:51200
	ds_read_b128 v[162:165], v177 offset:52224
	ds_read_b128 v[166:169], v177 offset:53248
	ds_read_b128 v[180:183], v177 offset:54272
	ds_read_b128 v[184:187], v177 offset:55296
	ds_read_b128 v[188:191], v177 offset:56320
	v_mov_b32_e32 v209, v147
	v_lshl_add_u64 v[210:211], s[36:37], 0, v[146:147]
	s_mov_b32 m0, s48
	v_lshl_add_u64 v[210:211], v[210:211], 0, s[12:13]
	v_lshl_add_u64 v[208:209], s[36:37], 0, v[208:209]
	global_load_lds_dwordx4 v[210:211], off
	v_lshl_add_u64 v[208:209], v[208:209], 0, s[12:13]
	s_mov_b32 m0, s49
	s_nop 0
	global_load_lds_dwordx4 v[208:209], off
	s_barrier
; __device__ __forceinline__ float bf_lo(unsigned w) { return __uint_as_float(w << 16); }
; __device__ __forceinline__ float bf_hi(unsigned w) { return __uint_as_float(w & 0xffff0000u); }
; __device__ __forceinline__ float sigmoidf_(float x) { return __builtin_amdgcn_rcpf(1.0f + __expf(-x)); }
; #define G8_STAGE(bufoff, gbase, v0, v1) do { unsigned x0_ = (v0), x1_ = (v1); asm volatile("" : "+v"(x0_), "+v"(x1_));     \
;         __builtin_amdgcn_global_load_lds((const unsigned*)((gbase) + x0_), (LAS unsigned*)(lds + (bufoff) + ldsw), 16, 0, 0); \
;         __builtin_amdgcn_global_load_lds((const unsigned*)((gbase) + x1_), (LAS unsigned*)(lds + (bufoff) + ldsw + 8192), 16, 0, 0); } while (0)
; #define G8_WAIT_V(n) asm volatile("s_waitcnt vmcnt(" #n ")" ::: "memory")
; #define G8_WAIT_L(n) asm volatile("s_waitcnt lgkmcnt(" #n ")" ::: "memory")
; #define G8_BAR __builtin_amdgcn_s_barrier()
;     ...
;             G8_BAR; G8_WAIT_L(0); if (do1) G8_MMA(1, 0, At, B0); G8_BAR; G8_SCHED;
;             G8_STAGE(G8_SB(1, 1), b3 + hstepB, voffB[0], voffB[1]);
;             G8_WAIT_V(6); G8_BAR; if (do1) G8_MMA(1, 1, At, B1); G8_BAR;
;         }
;     __device__ __forceinline__ void operator()(g8::Acc& acc, const g8::Unit& u, int wr, int wc, int fr, int fq) const {
;         const int row0 = u.pm * 256 + wr * 64 + fr, col0 = u.pn * 256 + wc * 32 + 8 * fq;
; #pragma unroll
;         for (int ai = 0; ai < 2; ++ai) {
;             u32x4 zz[4][2];
; #pragma unroll
;             for (int m = 0; m < 4; ++m)
; #pragma unroll
;                 for (int bj = 0; bj < 2; ++bj) zz[m][bj] = *(const u32x4*)(Z + (size_t)(row0 + ai * 128 + m * 16) * 1024 + col0 + bj * 128);
; #pragma unroll
;             for (int m = 0; m < 4; ++m) { const int row = row0 + ai * 128 + m * 16; float ss = 0.f;
; #pragma unroll
;                 for (int bj = 0; bj < 2; ++bj) { const f32x4 v0 = acc[ai][bj][m][0], v1 = acc[ai][bj][m][1];
;                     const u32x4 z4 = zz[m][bj];
;                     float o[8];
;                     o[0] = bf_lo(z4.x) * sigmoidf_(v0[0]); o[1] = bf_hi(z4.x) * sigmoidf_(v0[1]); o[2] = bf_lo(z4.y) * sigmoidf_(v0[2]); o[3] = bf_hi(z4.y) * sigmoidf_(v0[3]);
;                     o[4] = bf_lo(z4.z) * sigmoidf_(v1[0]); o[5] = bf_hi(z4.z) * sigmoidf_(v1[1]); o[6] = bf_lo(z4.w) * sigmoidf_(v1[2]); o[7] = bf_hi(z4.w) * sigmoidf_(v1[3]);
	s_waitcnt lgkmcnt(0)
	s_nop 0
	s_waitcnt lgkmcnt(0)
	v_mfma_f32_16x16x32_bf16 v[62:65], v[130:133], v[150:153], v[62:65]
	v_mfma_f32_16x16x32_bf16 v[58:61], v[138:141], v[150:153], v[58:61]
	v_mfma_f32_16x16x32_bf16 v[46:49], v[130:133], v[158:161], v[46:49]
	v_mfma_f32_16x16x32_bf16 v[42:45], v[138:141], v[158:161], v[42:45]
	v_mfma_f32_16x16x32_bf16 v[30:33], v[130:133], v[166:169], v[30:33]
	v_mfma_f32_16x16x32_bf16 v[26:29], v[138:141], v[166:169], v[26:29]
	v_mfma_f32_16x16x32_bf16 v[14:17], v[130:133], v[184:187], v[14:17]
	v_mfma_f32_16x16x32_bf16 v[10:13], v[138:141], v[184:187], v[10:13]
	v_mfma_f32_16x16x32_bf16 v[62:65], v[134:137], v[154:157], v[62:65]
	v_mfma_f32_16x16x32_bf16 v[58:61], v[142:145], v[154:157], v[58:61]
	v_mfma_f32_16x16x32_bf16 v[46:49], v[134:137], v[162:165], v[46:49]
	v_mfma_f32_16x16x32_bf16 v[42:45], v[142:145], v[162:165], v[42:45]
	v_mfma_f32_16x16x32_bf16 v[30:33], v[134:137], v[180:183], v[30:33]
	v_mfma_f32_16x16x32_bf16 v[26:29], v[142:145], v[180:183], v[26:29]
	v_mfma_f32_16x16x32_bf16 v[14:17], v[134:137], v[188:191], v[14:17]
	v_mfma_f32_16x16x32_bf16 v[10:13], v[142:145], v[188:191], v[10:13]
	s_nop 0
	s_barrier
	s_add_u32 s34, s34, 0xc000
	s_addc_u32 s35, s35, 0
	s_add_i32 s36, s66, s40
	v_mov_b32_e32 v130, v171
	v_mov_b32_e32 v131, v170
	s_mov_b32 m0, s36
	s_nop 0
	global_load_lds_dwordx4 v131, s[34:35]
	s_add_i32 m0, s36, 0x2000
	s_nop 0
	global_load_lds_dwordx4 v130, s[34:35]
	s_waitcnt vmcnt(6)
	s_barrier
	s_nop 0
	v_mfma_f32_16x16x32_bf16 v[54:57], v[192:195], v[150:153], v[54:57]
	v_mfma_f32_16x16x32_bf16 v[50:53], v[200:203], v[150:153], v[50:53]
	v_mfma_f32_16x16x32_bf16 v[38:41], v[192:195], v[158:161], v[38:41]
	v_mfma_f32_16x16x32_bf16 v[34:37], v[200:203], v[158:161], v[34:37]
	v_mfma_f32_16x16x32_bf16 v[22:25], v[192:195], v[166:169], v[22:25]
	v_mfma_f32_16x16x32_bf16 v[18:21], v[200:203], v[166:169], v[18:21]
	v_mfma_f32_16x16x32_bf16 v[6:9], v[192:195], v[184:187], v[6:9]
	v_mfma_f32_16x16x32_bf16 v[2:5], v[200:203], v[184:187], v[2:5]
	v_mfma_f32_16x16x32_bf16 v[54:57], v[196:199], v[154:157], v[54:57]
	v_mfma_f32_16x16x32_bf16 v[50:53], v[204:207], v[154:157], v[50:53]
	v_mfma_f32_16x16x32_bf16 v[38:41], v[196:199], v[162:165], v[38:41]
	v_mfma_f32_16x16x32_bf16 v[34:37], v[204:207], v[162:165], v[34:37]
	v_mfma_f32_16x16x32_bf16 v[22:25], v[196:199], v[180:183], v[22:25]
	v_mfma_f32_16x16x32_bf16 v[18:21], v[204:207], v[180:183], v[18:21]
	v_mfma_f32_16x16x32_bf16 v[6:9], v[196:199], v[188:191], v[6:9]
	v_mfma_f32_16x16x32_bf16 v[2:5], v[204:207], v[188:191], v[2:5]
	s_nop 0
	s_add_i32 s64, s64, 2
	s_cmp_gt_u32 s64, 13
	s_barrier
	s_cbranch_scc0 .LBB0_536
	s_mov_b32 s0, 0
	v_mul_f32_e32 v126, 0xbfb8aa3b, v126
	v_mbcnt_lo_u32_b32 v130, -1, s0
	s_lshl_b32 s0, s60, 8
	v_mbcnt_hi_u32_b32 v132, -1, v130
	s_add_i32 s0, s0, s46
	v_and_or_b32 v154, v132, 15, s0
	s_lshl_b32 s0, s59, 8
	v_lshrrev_b32_e32 v130, 1, v132
	s_or_b32 s0, s0, s47
	v_and_b32_e32 v130, 0x7ffffff8, v130
	v_add_u32_e32 v150, s0, v130
	v_ashrrev_i32_e32 v151, 31, v150
	v_ashrrev_i32_e32 v155, 31, v154
	v_lshl_add_u64 v[152:153], v[150:151], 1, s[4:5]
	v_lshlrev_b64 v[168:169], 11, v[154:155]
	v_lshl_add_u64 v[130:131], v[152:153], 0, v[168:169]
	global_load_dwordx4 v[182:185], v[130:131], off
	global_load_dwordx4 v[186:189], v[130:131], off offset:256
	v_mul_f32_e32 v122, 0xbfb8aa3b, v122
	v_mul_f32_e32 v123, 0xbfb8aa3b, v123
	v_mul_f32_e32 v124, 0xbfb8aa3b, v124
	v_and_b32_e32 v134, 64, v179
	v_mul_f32_e32 v127, 0xbfb8aa3b, v127
	v_mul_f32_e32 v128, 0xbfb8aa3b, v128
	v_mul_f32_e32 v129, 0xbfb8aa3b, v129
	v_exp_f32_e32 v126, v126
	v_exp_f32_e32 v122, v122
	v_exp_f32_e32 v123, v123
	v_exp_f32_e32 v124, v124
	v_xor_b32_e32 v133, 16, v179
	v_add_u32_e32 v134, 64, v134
	v_exp_f32_e32 v127, v127
	v_exp_f32_e32 v128, v128
	v_exp_f32_e32 v129, v129
	v_mul_f32_e32 v125, 0xbfb8aa3b, v125
	v_cmp_lt_i32_e32 vcc, v133, v134
	v_or_b32_e32 v164, 16, v154
	v_or_b32_e32 v160, 32, v154
	v_xor_b32_e32 v135, 32, v179
	v_exp_f32_e32 v181, v125
	v_cndmask_b32_e32 v125, v179, v133, vcc
	v_or_b32_e32 v156, 48, v154
	v_ashrrev_i32_e32 v165, 31, v164
	v_ashrrev_i32_e32 v161, 31, v160
	v_cmp_lt_i32_e32 vcc, v135, v134
	v_lshlrev_b32_e32 v180, 2, v125
	v_add_f32_e32 v125, 1.0, v126
	v_add_f32_e32 v122, 1.0, v122
	v_add_f32_e32 v123, 1.0, v123
	v_add_f32_e32 v124, 1.0, v124
	v_ashrrev_i32_e32 v157, 31, v156
	v_lshlrev_b64 v[166:167], 11, v[164:165]
	v_lshlrev_b64 v[162:163], 11, v[160:161]
	v_cndmask_b32_e32 v133, v179, v135, vcc
	v_add_f32_e32 v126, 1.0, v127
	v_add_f32_e32 v127, 1.0, v128
	v_add_f32_e32 v128, 1.0, v129
	v_rcp_f32_e32 v192, v125
	v_rcp_f32_e32 v196, v122
	v_rcp_f32_e32 v197, v123
	v_rcp_f32_e32 v198, v124
	v_lshlrev_b64 v[158:159], 11, v[156:157]
	v_lshl_add_u64 v[122:123], v[152:153], 0, v[166:167]
	v_lshl_add_u64 v[124:125], v[152:153], 0, v[162:163]
	v_lshlrev_b32_e32 v146, 2, v133
	v_cmp_gt_u32_e32 vcc, 16, v132
	v_rcp_f32_e32 v193, v126
	v_rcp_f32_e32 v194, v127
	v_rcp_f32_e32 v195, v128
	v_lshl_add_u64 v[190:191], v[152:153], 0, v[158:159]
	global_load_dwordx4 v[142:145], v[122:123], off
	global_load_dwordx4 v[138:141], v[122:123], off offset:256
	global_load_dwordx4 v[134:137], v[124:125], off
	global_load_dwordx4 v[130:133], v[124:125], off offset:256
	global_load_dwordx4 v[126:129], v[190:191], off
	s_nop 0
	global_load_dwordx4 v[122:125], v[190:191], off offset:256
	v_add_f32_e32 v181, 1.0, v181
	v_rcp_f32_e32 v181, v181
	v_mul_f32_e32 v118, 0xbfb8aa3b, v118
	v_exp_f32_e32 v118, v118
	v_mul_f32_e32 v119, 0xbfb8aa3b, v119
	v_exp_f32_e32 v119, v119
	v_mul_f32_e32 v120, 0xbfb8aa3b, v120
	v_exp_f32_e32 v120, v120
	v_mul_f32_e32 v121, 0xbfb8aa3b, v121
	v_exp_f32_e32 v121, v121
	v_mul_f32_e32 v114, 0xbfb8aa3b, v114
	v_add_f32_e32 v118, 1.0, v118
	v_exp_f32_e32 v114, v114
	v_mul_f32_e32 v115, 0xbfb8aa3b, v115
	v_rcp_f32_e32 v118, v118
	v_add_f32_e32 v119, 1.0, v119
	v_exp_f32_e32 v115, v115
	v_mul_f32_e32 v116, 0xbfb8aa3b, v116
	v_rcp_f32_e32 v119, v119
	v_add_f32_e32 v120, 1.0, v120
	v_exp_f32_e32 v116, v116
	v_mul_f32_e32 v117, 0xbfb8aa3b, v117
	v_rcp_f32_e32 v120, v120
	v_add_f32_e32 v121, 1.0, v121
	v_exp_f32_e32 v117, v117
	s_waitcnt vmcnt(0)
; __device__ __forceinline__ float bf_lo(unsigned w) { return __uint_as_float(w << 16); }
; __device__ __forceinline__ float bf_hi(unsigned w) { return __uint_as_float(w & 0xffff0000u); }
; __device__ __forceinline__ float sigmoidf_(float x) { return __builtin_amdgcn_rcpf(1.0f + __expf(-x)); }
;     __device__ __forceinline__ void operator()(g8::Acc& acc, const g8::Unit& u, int wr, int wc, int fr, int fq) const {
;     ...
;             for (int m = 0; m < 4; ++m) { const int row = row0 + ai * 128 + m * 16; float ss = 0.f;
; #pragma unroll
;                 for (int bj = 0; bj < 2; ++bj) { const f32x4 v0 = acc[ai][bj][m][0], v1 = acc[ai][bj][m][1];
;                     const u32x4 z4 = zz[m][bj];
;                     float o[8];
;                     o[0] = bf_lo(z4.x) * sigmoidf_(v0[0]); o[1] = bf_hi(z4.x) * sigmoidf_(v0[1]); o[2] = bf_lo(z4.y) * sigmoidf_(v0[2]); o[3] = bf_hi(z4.y) * sigmoidf_(v0[3]);
;                     o[4] = bf_lo(z4.z) * sigmoidf_(v1[0]); o[5] = bf_hi(z4.z) * sigmoidf_(v1[1]); o[6] = bf_lo(z4.w) * sigmoidf_(v1[2]); o[7] = bf_hi(z4.w) * sigmoidf_(v1[3]);
; #pragma unroll
;                     for (int j = 0; j < 8; ++j) ss += o[j] * o[j];
;                     int wa = 0, wb = 0;
;                     wa = __builtin_amdgcn_cvt_pk_fp8_f32(o[0] * CAT_SCALE, o[1] * CAT_SCALE, wa, false); wa = __builtin_amdgcn_cvt_pk_fp8_f32(o[2] * CAT_SCALE, o[3] * CAT_SCALE, wa, true);
;                     wb = __builtin_amdgcn_cvt_pk_fp8_f32(o[4] * CAT_SCALE, o[5] * CAT_SCALE, wb, false); wb = __builtin_amdgcn_cvt_pk_fp8_f32(o[6] * CAT_SCALE, o[7] * CAT_SCALE, wb, true);
;                     u32x2 w; w.x = (unsigned)wa; w.y = (unsigned)wb;
;                     __hip_atomic_store((unsigned long long*)(CAT + (size_t)row * DM + col0 + bj * 128), __builtin_bit_cast(unsigned long long, w), __ATOMIC_RELAXED, __HIP_MEMORY_SCOPE_AGENT); }
;                 ss += __shfl_xor(ss, 16); ss += __shfl_xor(ss, 32);
;                 if (fq == 0) __hip_atomic_store(&rowss[(size_t)row * 16 + u.pn * 4 + wc], ss, __ATOMIC_RELAXED, __HIP_MEMORY_SCOPE_AGENT); }
	v_lshlrev_b32_e32 v190, 16, v182
	v_and_b32_e32 v182, 0xffff0000, v182
	v_mul_f32_e32 v182, v193, v182
	v_lshlrev_b32_e32 v193, 16, v185
	v_and_b32_e32 v185, 0xffff0000, v185
	v_lshlrev_b32_e32 v191, 16, v183
	v_mul_f32_e32 v190, v192, v190
	v_mul_f32_e32 v181, v181, v185
	v_mul_f32_e32 v185, v182, v182
	v_mul_f32_e32 v191, v194, v191
	v_fmac_f32_e32 v185, v190, v190
	v_mul_f32_e32 v190, 0x41000000, v190
	v_mul_f32_e32 v194, 0x41000000, v182
	v_mov_b32_e32 v182, v147
	v_and_b32_e32 v183, 0xffff0000, v183
	v_cvt_pk_fp8_f32 v182, v190, v194
	v_lshlrev_b32_e32 v199, 16, v184
	v_mul_f32_e32 v183, v195, v183
	v_fmac_f32_e32 v185, v191, v191
	v_and_b32_e32 v184, 0xffff0000, v184
	v_mul_f32_e32 v192, v196, v199
	v_fmac_f32_e32 v185, v183, v183
	v_mul_f32_e32 v184, v197, v184
	v_fmac_f32_e32 v185, v192, v192
	v_mul_f32_e32 v190, 0x41000000, v191
	v_mul_f32_e32 v183, 0x41000000, v183
	v_fmac_f32_e32 v185, v184, v184
	v_cvt_pk_fp8_f32 v182, v190, v183 op_sel:[0,0,1]
	v_mul_f32_e32 v190, 0x41000000, v192
	v_mul_f32_e32 v184, 0x41000000, v184
	v_mov_b32_e32 v183, v147
	v_cvt_pk_fp8_f32 v183, v190, v184
	v_mul_f32_e32 v193, v198, v193
	v_fmac_f32_e32 v185, v193, v193
	v_fmac_f32_e32 v185, v181, v181
	v_mul_f32_e32 v184, 0x41000000, v193
	v_mul_f32_e32 v181, 0x41000000, v181
	v_cvt_pk_fp8_f32 v183, v184, v181 op_sel:[0,0,1]
	v_lshlrev_b32_e32 v181, 16, v186
	v_rcp_f32_e32 v121, v121
	v_add_f32_e32 v114, 1.0, v114
	v_mul_f32_e32 v118, v118, v181
	v_and_b32_e32 v181, 0xffff0000, v186
	v_rcp_f32_e32 v114, v114
	v_add_f32_e32 v115, 1.0, v115
	v_mul_f32_e32 v119, v119, v181
	v_lshlrev_b32_e32 v181, 16, v187
	v_rcp_f32_e32 v115, v115
	v_add_f32_e32 v116, 1.0, v116
	v_fmac_f32_e32 v185, v118, v118
	v_mul_f32_e32 v120, v120, v181
	v_and_b32_e32 v181, 0xffff0000, v187
	v_rcp_f32_e32 v116, v116
	v_add_f32_e32 v117, 1.0, v117
	v_fmac_f32_e32 v185, v119, v119
	v_mul_f32_e32 v121, v121, v181
	v_lshlrev_b32_e32 v181, 16, v188
	v_rcp_f32_e32 v117, v117
	v_fmac_f32_e32 v185, v120, v120
	v_mul_f32_e32 v114, v114, v181
	v_and_b32_e32 v181, 0xffff0000, v188
	v_fmac_f32_e32 v185, v121, v121
	v_mul_f32_e32 v115, v115, v181
	v_lshlrev_b32_e32 v181, 16, v189
	v_fmac_f32_e32 v185, v114, v114
	v_mul_f32_e32 v181, v116, v181
	v_and_b32_e32 v116, 0xffff0000, v189
	v_fmac_f32_e32 v185, v115, v115
	v_mul_f32_e32 v184, v117, v116
	v_fmac_f32_e32 v185, v181, v181
	v_mul_f32_e32 v117, 0x41000000, v118
	v_mul_f32_e32 v118, 0x41000000, v119
	v_mov_b32_e32 v116, v147
	v_fmac_f32_e32 v185, v184, v184
	v_cvt_pk_fp8_f32 v116, v117, v118
	v_mul_f32_e32 v114, 0x41000000, v114
	v_mul_f32_e32 v115, 0x41000000, v115
	v_mov_b32_e32 v117, v147
	v_cvt_pk_fp8_f32 v117, v114, v115
	ds_bpermute_b32 v114, v180, v185
	v_mul_f32_e32 v118, 0x41000000, v120
	v_mul_f32_e32 v119, 0x41000000, v121
	v_cvt_pk_fp8_f32 v116, v118, v119 op_sel:[0,0,1]
	v_mul_f32_e32 v115, 0x41000000, v181
	v_mul_f32_e32 v118, 0x41000000, v184
	s_waitcnt lgkmcnt(0)
	v_add_f32_e32 v114, v185, v114
	v_cvt_pk_fp8_f32 v117, v115, v118 op_sel:[0,0,1]
	ds_bpermute_b32 v115, v146, v114
	s_lshl_b32 s28, s59, 2
	v_lshl_add_u64 v[118:119], s[8:9], 0, v[168:169]
	s_ashr_i32 s29, s28, 31
	v_lshl_add_u64 v[118:119], v[118:119], 0, v[150:151]
	global_store_dwordx2 v[118:119], v[182:183], off sc1
	global_store_dwordx2 v[118:119], v[116:117], off offset:128 sc1
	s_and_saveexec_b64 s[30:31], vcc
	s_cbranch_execz .LBB0_539
	s_waitcnt lgkmcnt(0)
	v_add_f32_e32 v116, v114, v115
	v_lshlrev_b64 v[114:115], 6, v[154:155]
	v_lshl_add_u64 v[114:115], s[10:11], 0, v[114:115]
	v_lshl_add_u64 v[114:115], s[28:29], 2, v[114:115]
	s_lshl_b32 s0, s45, 2
	v_lshl_add_u64 v[114:115], v[114:115], 0, s[0:1]
	global_store_dword v[114:115], v116, off sc1

; #define G8_STAGE(bufoff, gbase, v0, v1) do { unsigned x0_ = (v0), x1_ = (v1); asm volatile("" : "+v"(x0_), "+v"(x1_));     \
;         __builtin_amdgcn_global_load_lds((const unsigned*)((gbase) + x0_), (LAS unsigned*)(lds + (bufoff) + ldsw), 16, 0, 0); \
;         __builtin_amdgcn_global_load_lds((const unsigned*)((gbase) + x1_), (LAS unsigned*)(lds + (bufoff) + ldsw + 8192), 16, 0, 0); } while (0)
; #define G8_LDA(dst, b, h) do { _Pragma("unroll") for (int m = 0; m < 4; ++m) _Pragma("unroll") for (int k = 0; k < 2; ++k) dst[m][k] = *(const LAS bf16x8*)(lds + G8_SA(b, h) + aoff + m * 2048 + k * 1024); } while (0)
; #define G8_LDB(dst, b, h) do { _Pragma("unroll") for (int n = 0; n < 2; ++n) _Pragma("unroll") for (int k = 0; k < 2; ++k) dst[n][k] = *(const LAS bf16x8*)(lds + G8_SB(b, h) + boff + n * 2048 + k * 1024); } while (0)
; #define G8_WAIT_V(n) asm volatile("s_waitcnt vmcnt(" #n ")" ::: "memory")
; #define G8_WAIT_L(n) asm volatile("s_waitcnt lgkmcnt(" #n ")" ::: "memory")
; #define G8_BAR __builtin_amdgcn_s_barrier()
; #define G8_SCHED __builtin_amdgcn_sched_barrier(0)
;     ...
;             G8_CONV_READ; G8_SCHED;
;             G8_LDB(B0, 0, 0); G8_SCHED; G8_LDA(At, 0, 0); G8_STAGE(G8_SA(1, 1), a1, cv[1][0], cv[1][1]);
;             G8_WAIT_L(8); G8_BAR; G8_WAIT_L(0); if (do0) G8_MMA(0, 0, At, B0); G8_CONV_CVT; G8_BAR; G8_SCHED;
;             G8_LDB(B1, 0, 1); G8_STAGE(G8_SB(0, 0), b2, voffB[0], voffB[1]);
;             G8_BAR; G8_CONV_ISSUE;
;             G8_WAIT_L(0); if (do0) G8_MMA(0, 1, At, B1); G8_BAR;
;             G8_LDA(At, 0, 1); G8_STAGE(G8_SA(0, 0), a2, o00, o01);
;             G8_BAR; G8_WAIT_L(0); if (do1) G8_MMA(1, 0, At, B0); G8_BAR; G8_SCHED;
;             G8_STAGE(G8_SB(0, 1), b2 + hstepB, voffB[0], voffB[1]);
;             if constexpr (CONV) G8_WAIT_V(9); else G8_WAIT_V(6);
;             G8_BAR; if (do1) G8_MMA(1, 1, At, B1); G8_BAR;
;             G8_LDB(B0, 1, 0); G8_SCHED; G8_LDA(At, 1, 0); G8_STAGE(G8_SA(0, 1), a2, o10, o11);
.LBB0_741:
	s_add_u32 s70, s0, 0x80
	s_addc_u32 s71, s1, 0
	s_add_u32 s0, s0, 0x100
	s_addc_u32 s1, s1, 0
	s_add_u32 s34, s34, 0x10000
	s_addc_u32 s35, s35, 0
	s_cmp_eq_u32 s68, 4
	s_cselect_b32 s39, s64, s1
	s_cselect_b32 s38, s65, s0
	s_cselect_b32 s37, s66, s35
	s_cselect_b32 s36, s67, s34
	v_add_u32_e32 v2, s51, v183
	ds_read_b128 v[134:137], v2
	ds_read_b128 v[138:141], v2 offset:1024
	ds_read_b128 v[142:145], v2 offset:2048
	ds_read_b128 v[146:149], v2 offset:3072
	v_mov_b32_e32 v2, v182
	v_mov_b32_e32 v4, v181
	s_add_i32 m0, s41, 0xc000
	ds_read_b128 v[154:157], v184
	ds_read_b128 v[158:161], v184 offset:1024
	ds_read_b128 v[162:165], v184 offset:2048
	ds_read_b128 v[166:169], v184 offset:3072
	ds_read_b128 v[170:173], v184 offset:4096
	ds_read_b128 v[174:177], v184 offset:5120
	ds_read_b128 v[188:191], v184 offset:6144
	ds_read_b128 v[192:195], v184 offset:7168
	s_nop 0
	global_load_lds_dwordx4 v4, s[70:71]
	s_add_i32 m0, s41, 0xe000
	s_nop 0
	global_load_lds_dwordx4 v2, s[70:71]
	s_waitcnt lgkmcnt(8)
	s_barrier
	s_waitcnt lgkmcnt(0)
	s_nop 0
	s_waitcnt lgkmcnt(0)
	v_mfma_scale_f32_16x16x128_f8f6f4 v[196:199], v[134:141], v[154:161], v[6:9], v185, v185 op_sel_hi:[0,0,0]
	v_mfma_scale_f32_16x16x128_f8f6f4 v[200:203], v[142:149], v[154:161], v[10:13], v185, v185 op_sel_hi:[0,0,0]
	v_mfma_scale_f32_16x16x128_f8f6f4 v[204:207], v[134:141], v[162:169], v[14:17], v185, v185 op_sel_hi:[0,0,0]
	v_mfma_scale_f32_16x16x128_f8f6f4 v[208:211], v[142:149], v[162:169], v[18:21], v185, v185 op_sel_hi:[0,0,0]
	v_mfma_scale_f32_16x16x128_f8f6f4 v[212:215], v[134:141], v[170:177], v[22:25], v185, v185 op_sel_hi:[0,0,0]
	v_mfma_scale_f32_16x16x128_f8f6f4 v[216:219], v[142:149], v[170:177], v[26:29], v185, v185 op_sel_hi:[0,0,0]
	v_mfma_scale_f32_16x16x128_f8f6f4 v[220:223], v[134:141], v[188:195], v[30:33], v185, v185 op_sel_hi:[0,0,0]
	v_mfma_scale_f32_16x16x128_f8f6f4 v[224:227], v[142:149], v[188:195], v[34:37], v185, v185 op_sel_hi:[0,0,0]
	s_nop 0
	s_barrier
	v_add_u32_e32 v2, s52, v183
	s_add_i32 s69, s51, s40
	ds_read_b128 v[4:7], v2
	ds_read_b128 v[8:11], v2 offset:1024
	ds_read_b128 v[12:15], v2 offset:2048
	ds_read_b128 v[16:19], v2 offset:3072
	v_mov_b32_e32 v2, v178
	v_mov_b32_e32 v20, v1
	s_mov_b32 m0, s69
	s_nop 0
	global_load_lds_dwordx4 v20, s[36:37]
	s_add_i32 m0, s69, 0x2000
	s_nop 0
	global_load_lds_dwordx4 v2, s[36:37]
	s_barrier
	s_waitcnt lgkmcnt(0)
	s_nop 0
	s_waitcnt lgkmcnt(0)
	v_mfma_scale_f32_16x16x128_f8f6f4 v[228:231], v[4:11], v[154:161], v[38:41], v185, v185 op_sel_hi:[0,0,0]
	v_mfma_scale_f32_16x16x128_f8f6f4 v[232:235], v[12:19], v[154:161], v[42:45], v185, v185 op_sel_hi:[0,0,0]
	v_mfma_scale_f32_16x16x128_f8f6f4 v[236:239], v[4:11], v[162:169], v[46:49], v185, v185 op_sel_hi:[0,0,0]
	v_mfma_scale_f32_16x16x128_f8f6f4 v[240:243], v[12:19], v[162:169], v[50:53], v185, v185 op_sel_hi:[0,0,0]
	v_mfma_scale_f32_16x16x128_f8f6f4 v[244:247], v[4:11], v[170:177], v[54:57], v185, v185 op_sel_hi:[0,0,0]
	v_mfma_scale_f32_16x16x128_f8f6f4 v[170:173], v[12:19], v[170:177], v[58:61], v185, v185 op_sel_hi:[0,0,0]
	v_mfma_scale_f32_16x16x128_f8f6f4 v[174:177], v[4:11], v[188:195], v[62:65], v185, v185 op_sel_hi:[0,0,0]
	v_mfma_scale_f32_16x16x128_f8f6f4 v[188:191], v[12:19], v[188:195], v[66:69], v185, v185 op_sel_hi:[0,0,0]
	s_nop 0
	v_mov_b32_e32 v2, v179
	s_nop 0
	v_mov_b32_e32 v52, v180
	s_mov_b32 m0, s41
	s_barrier
	ds_read_b128 v[20:23], v184 offset:16384
	ds_read_b128 v[24:27], v184 offset:17408
	ds_read_b128 v[28:31], v184 offset:18432
	ds_read_b128 v[32:35], v184 offset:19456
	ds_read_b128 v[36:39], v184 offset:20480
	ds_read_b128 v[40:43], v184 offset:21504
	ds_read_b128 v[44:47], v184 offset:22528
	ds_read_b128 v[48:51], v184 offset:23552
	s_nop 0
	global_load_lds_dwordx4 v2, s[38:39]
	s_mov_b32 m0, s42
	s_nop 0
	global_load_lds_dwordx4 v52, s[38:39]
	s_barrier
	s_waitcnt lgkmcnt(0)
	s_nop 0
	s_waitcnt lgkmcnt(0)
	v_mfma_scale_f32_16x16x128_f8f6f4 v[74:77], v[142:149], v[20:27], v[74:77], v185, v185 op_sel_hi:[0,0,0]
	v_mfma_scale_f32_16x16x128_f8f6f4 v[78:81], v[134:141], v[28:35], v[78:81], v185, v185 op_sel_hi:[0,0,0]
	v_mfma_scale_f32_16x16x128_f8f6f4 v[82:85], v[142:149], v[28:35], v[82:85], v185, v185 op_sel_hi:[0,0,0]
	v_mfma_scale_f32_16x16x128_f8f6f4 v[86:89], v[134:141], v[36:43], v[86:89], v185, v185 op_sel_hi:[0,0,0]
	v_mfma_scale_f32_16x16x128_f8f6f4 v[90:93], v[142:149], v[36:43], v[90:93], v185, v185 op_sel_hi:[0,0,0]
	v_mfma_scale_f32_16x16x128_f8f6f4 v[94:97], v[134:141], v[44:51], v[94:97], v185, v185 op_sel_hi:[0,0,0]
	v_mfma_scale_f32_16x16x128_f8f6f4 v[98:101], v[142:149], v[44:51], v[98:101], v185, v185 op_sel_hi:[0,0,0]
	v_mfma_scale_f32_16x16x128_f8f6f4 v[248:251], v[134:141], v[20:27], v[70:73], v185, v185 op_sel_hi:[0,0,0]
	s_nop 0
	s_barrier
	s_add_u32 s70, s36, 0x4000
	s_addc_u32 s71, s37, 0
	s_add_i32 s69, s52, s40
	v_mov_b32_e32 v2, v178
	v_mov_b32_e32 v52, v1
	s_mov_b32 m0, s69
	s_nop 0
	global_load_lds_dwordx4 v52, s[70:71]
	s_add_i32 m0, s69, 0x2000
	s_nop 0
	global_load_lds_dwordx4 v2, s[70:71]
	s_waitcnt vmcnt(6)
	s_barrier
	s_nop 0
	v_mfma_scale_f32_16x16x128_f8f6f4 v[102:105], v[4:11], v[20:27], v[102:105], v185, v185 op_sel_hi:[0,0,0]
	v_mfma_scale_f32_16x16x128_f8f6f4 v[106:109], v[12:19], v[20:27], v[106:109], v185, v185 op_sel_hi:[0,0,0]
	v_mfma_scale_f32_16x16x128_f8f6f4 v[110:113], v[4:11], v[28:35], v[110:113], v185, v185 op_sel_hi:[0,0,0]
	v_mfma_scale_f32_16x16x128_f8f6f4 v[114:117], v[12:19], v[28:35], v[114:117], v185, v185 op_sel_hi:[0,0,0]
	v_mfma_scale_f32_16x16x128_f8f6f4 v[118:121], v[4:11], v[36:43], v[118:121], v185, v185 op_sel_hi:[0,0,0]
	v_mfma_scale_f32_16x16x128_f8f6f4 v[122:125], v[12:19], v[36:43], v[122:125], v185, v185 op_sel_hi:[0,0,0]
	v_mfma_scale_f32_16x16x128_f8f6f4 v[126:129], v[4:11], v[44:51], v[126:129], v185, v185 op_sel_hi:[0,0,0]
	v_mfma_scale_f32_16x16x128_f8f6f4 v[130:133], v[12:19], v[44:51], v[130:133], v185, v185 op_sel_hi:[0,0,0]
	s_nop 0
	s_add_i32 s69, 0, 0x18000
	v_add_u32_e32 v2, s69, v183
	s_barrier
; #define G8_STAGE(bufoff, gbase, v0, v1) do { unsigned x0_ = (v0), x1_ = (v1); asm volatile("" : "+v"(x0_), "+v"(x1_));     \
;         __builtin_amdgcn_global_load_lds((const unsigned*)((gbase) + x0_), (LAS unsigned*)(lds + (bufoff) + ldsw), 16, 0, 0); \
;         __builtin_amdgcn_global_load_lds((const unsigned*)((gbase) + x1_), (LAS unsigned*)(lds + (bufoff) + ldsw + 8192), 16, 0, 0); } while (0)
; #define G8_LDA(dst, b, h) do { _Pragma("unroll") for (int m = 0; m < 4; ++m) _Pragma("unroll") for (int k = 0; k < 2; ++k) dst[m][k] = *(const LAS bf16x8*)(lds + G8_SA(b, h) + aoff + m * 2048 + k * 1024); } while (0)
; #define G8_LDB(dst, b, h) do { _Pragma("unroll") for (int n = 0; n < 2; ++n) _Pragma("unroll") for (int k = 0; k < 2; ++k) dst[n][k] = *(const LAS bf16x8*)(lds + G8_SB(b, h) + boff + n * 2048 + k * 1024); } while (0)
; #define G8_WAIT_V(n) asm volatile("s_waitcnt vmcnt(" #n ")" ::: "memory")
; #define G8_WAIT_L(n) asm volatile("s_waitcnt lgkmcnt(" #n ")" ::: "memory")
; #define G8_BAR __builtin_amdgcn_s_barrier()
; #define G8_SCHED __builtin_amdgcn_sched_barrier(0)
;     ...
;             G8_LDB(B0, 1, 0); G8_SCHED; G8_LDA(At, 1, 0); G8_STAGE(G8_SA(0, 1), a2, o10, o11);
;             G8_WAIT_L(8); G8_BAR; G8_WAIT_L(0); if (do0) G8_MMA(0, 0, At, B0); G8_BAR; G8_SCHED;
;             G8_LDB(B1, 1, 1); G8_STAGE(G8_SB(1, 0), b3, voffB[0], voffB[1]);
;             G8_BAR; G8_WAIT_L(0); if (do0) G8_MMA(0, 1, At, B1); G8_BAR;
;             G8_LDA(At, 1, 1); G8_STAGE(G8_SA(1, 0), a3, o00, o01);
;             G8_BAR; G8_WAIT_L(0); if (do1) G8_MMA(1, 0, At, B0); G8_BAR; G8_SCHED;
;             G8_STAGE(G8_SB(1, 1), b3 + hstepB, voffB[0], voffB[1]);
;             G8_WAIT_V(6); G8_BAR; if (do1) G8_MMA(1, 1, At, B1); G8_BAR;
	ds_read_b128 v[134:137], v2
	ds_read_b128 v[138:141], v2 offset:1024
	ds_read_b128 v[142:145], v2 offset:2048
	ds_read_b128 v[146:149], v2 offset:3072
	v_mov_b32_e32 v2, v182
	v_mov_b32_e32 v4, v181
	s_mov_b32 m0, s43
	ds_read_b128 v[42:45], v184 offset:32768
	ds_read_b128 v[46:49], v184 offset:33792
	ds_read_b128 v[50:53], v184 offset:34816
	ds_read_b128 v[54:57], v184 offset:35840
	ds_read_b128 v[58:61], v184 offset:36864
	ds_read_b128 v[62:65], v184 offset:37888
	ds_read_b128 v[66:69], v184 offset:38912
	ds_read_b128 v[70:73], v184 offset:39936
	s_nop 0
	global_load_lds_dwordx4 v4, s[38:39]
	s_mov_b32 m0, s44
	s_nop 0
	global_load_lds_dwordx4 v2, s[38:39]
	s_waitcnt lgkmcnt(8)
	s_barrier
	s_waitcnt lgkmcnt(0)
	s_nop 0
	s_waitcnt lgkmcnt(0)
	v_mfma_scale_f32_16x16x128_f8f6f4 v[6:9], v[134:141], v[42:49], v[196:199], v185, v185 op_sel_hi:[0,0,0]
	v_mfma_scale_f32_16x16x128_f8f6f4 v[10:13], v[142:149], v[42:49], v[200:203], v185, v185 op_sel_hi:[0,0,0]
	v_mfma_scale_f32_16x16x128_f8f6f4 v[14:17], v[134:141], v[50:57], v[204:207], v185, v185 op_sel_hi:[0,0,0]
	v_mfma_scale_f32_16x16x128_f8f6f4 v[18:21], v[142:149], v[50:57], v[208:211], v185, v185 op_sel_hi:[0,0,0]
	v_mfma_scale_f32_16x16x128_f8f6f4 v[22:25], v[134:141], v[58:65], v[212:215], v185, v185 op_sel_hi:[0,0,0]
	v_mfma_scale_f32_16x16x128_f8f6f4 v[26:29], v[142:149], v[58:65], v[216:219], v185, v185 op_sel_hi:[0,0,0]
	v_mfma_scale_f32_16x16x128_f8f6f4 v[30:33], v[134:141], v[66:73], v[220:223], v185, v185 op_sel_hi:[0,0,0]
	v_mfma_scale_f32_16x16x128_f8f6f4 v[34:37], v[142:149], v[66:73], v[224:227], v185, v185 op_sel_hi:[0,0,0]
	s_nop 0
	s_barrier
	s_add_i32 s72, 0, 0x1c000
	s_add_u32 s70, s36, 0x8000
	v_add_u32_e32 v2, s72, v183
	s_addc_u32 s71, s37, 0
	s_add_i32 s69, s69, s40
	ds_read_b128 v[154:157], v2
	ds_read_b128 v[158:161], v2 offset:1024
	ds_read_b128 v[162:165], v2 offset:2048
	ds_read_b128 v[166:169], v2 offset:3072
	v_mov_b32_e32 v2, v1
	v_mov_b32_e32 v4, v178
	s_mov_b32 m0, s69
	s_nop 0
	global_load_lds_dwordx4 v2, s[70:71]
	s_add_i32 m0, s69, 0x2000
	s_nop 0
	global_load_lds_dwordx4 v4, s[70:71]
	s_barrier
	s_waitcnt lgkmcnt(0)
	s_nop 0
	s_waitcnt lgkmcnt(0)
	v_mfma_scale_f32_16x16x128_f8f6f4 v[38:41], v[154:161], v[42:49], v[228:231], v185, v185 op_sel_hi:[0,0,0]
	v_mfma_scale_f32_16x16x128_f8f6f4 v[42:45], v[162:169], v[42:49], v[232:235], v185, v185 op_sel_hi:[0,0,0]
	v_mfma_scale_f32_16x16x128_f8f6f4 v[46:49], v[154:161], v[50:57], v[236:239], v185, v185 op_sel_hi:[0,0,0]
	v_mfma_scale_f32_16x16x128_f8f6f4 v[50:53], v[162:169], v[50:57], v[240:243], v185, v185 op_sel_hi:[0,0,0]
	v_mfma_scale_f32_16x16x128_f8f6f4 v[54:57], v[154:161], v[58:65], v[244:247], v185, v185 op_sel_hi:[0,0,0]
	v_mfma_scale_f32_16x16x128_f8f6f4 v[58:61], v[162:169], v[58:65], v[170:173], v185, v185 op_sel_hi:[0,0,0]
	v_mfma_scale_f32_16x16x128_f8f6f4 v[62:65], v[154:161], v[66:73], v[174:177], v185, v185 op_sel_hi:[0,0,0]
	v_mfma_scale_f32_16x16x128_f8f6f4 v[66:69], v[162:169], v[66:73], v[188:191], v185, v185 op_sel_hi:[0,0,0]
	s_nop 0
	v_mov_b32_e32 v4, v180
	v_mov_b32_e32 v2, v179
	s_barrier
	s_nop 0
	ds_read_b128 v[170:173], v184 offset:49152
	ds_read_b128 v[174:177], v184 offset:50176
	ds_read_b128 v[188:191], v184 offset:51200
	ds_read_b128 v[192:195], v184 offset:52224
	ds_read_b128 v[196:199], v184 offset:53248
	ds_read_b128 v[200:203], v184 offset:54272
	ds_read_b128 v[204:207], v184 offset:55296
	ds_read_b128 v[208:211], v184 offset:56320
	v_mov_b32_e32 v5, v3
	v_lshl_add_u64 v[70:71], s[38:39], 0, v[2:3]
	s_mov_b32 m0, s48
	v_lshl_add_u64 v[70:71], v[70:71], 0, s[14:15]
	v_lshl_add_u64 v[4:5], s[38:39], 0, v[4:5]
	global_load_lds_dwordx4 v[70:71], off
	v_lshl_add_u64 v[4:5], v[4:5], 0, s[14:15]
	s_mov_b32 m0, s49
	s_nop 0
	global_load_lds_dwordx4 v[4:5], off
	s_barrier
	s_waitcnt lgkmcnt(0)
	s_nop 0
	s_waitcnt lgkmcnt(0)
	v_mfma_scale_f32_16x16x128_f8f6f4 v[70:73], v[134:141], v[170:177], v[248:251], v185, v185 op_sel_hi:[0,0,0]
	v_mfma_scale_f32_16x16x128_f8f6f4 v[74:77], v[142:149], v[170:177], v[74:77], v185, v185 op_sel_hi:[0,0,0]
	v_mfma_scale_f32_16x16x128_f8f6f4 v[78:81], v[134:141], v[188:195], v[78:81], v185, v185 op_sel_hi:[0,0,0]
	v_mfma_scale_f32_16x16x128_f8f6f4 v[82:85], v[142:149], v[188:195], v[82:85], v185, v185 op_sel_hi:[0,0,0]
	v_mfma_scale_f32_16x16x128_f8f6f4 v[86:89], v[134:141], v[196:203], v[86:89], v185, v185 op_sel_hi:[0,0,0]
	v_mfma_scale_f32_16x16x128_f8f6f4 v[90:93], v[142:149], v[196:203], v[90:93], v185, v185 op_sel_hi:[0,0,0]
	v_mfma_scale_f32_16x16x128_f8f6f4 v[94:97], v[134:141], v[204:211], v[94:97], v185, v185 op_sel_hi:[0,0,0]
	v_mfma_scale_f32_16x16x128_f8f6f4 v[98:101], v[142:149], v[204:211], v[98:101], v185, v185 op_sel_hi:[0,0,0]
	s_nop 0
	s_barrier
	s_add_u32 s36, s36, 0xc000
	s_addc_u32 s37, s37, 0
	s_add_i32 s38, s72, s40
	v_mov_b32_e32 v2, v178
	v_mov_b32_e32 v4, v1
	s_mov_b32 m0, s38
	s_nop 0
	global_load_lds_dwordx4 v4, s[36:37]
	s_add_i32 m0, s38, 0x2000
	s_nop 0
	global_load_lds_dwordx4 v2, s[36:37]
	s_waitcnt vmcnt(6)
	s_barrier
	s_nop 0
	v_mfma_scale_f32_16x16x128_f8f6f4 v[102:105], v[154:161], v[170:177], v[102:105], v185, v185 op_sel_hi:[0,0,0]
	v_mfma_scale_f32_16x16x128_f8f6f4 v[106:109], v[162:169], v[170:177], v[106:109], v185, v185 op_sel_hi:[0,0,0]
	v_mfma_scale_f32_16x16x128_f8f6f4 v[110:113], v[154:161], v[188:195], v[110:113], v185, v185 op_sel_hi:[0,0,0]
	v_mfma_scale_f32_16x16x128_f8f6f4 v[114:117], v[162:169], v[188:195], v[114:117], v185, v185 op_sel_hi:[0,0,0]
	v_mfma_scale_f32_16x16x128_f8f6f4 v[118:121], v[154:161], v[196:203], v[118:121], v185, v185 op_sel_hi:[0,0,0]
	v_mfma_scale_f32_16x16x128_f8f6f4 v[122:125], v[162:169], v[196:203], v[122:125], v185, v185 op_sel_hi:[0,0,0]
	v_mfma_scale_f32_16x16x128_f8f6f4 v[126:129], v[154:161], v[204:211], v[126:129], v185, v185 op_sel_hi:[0,0,0]
	v_mfma_scale_f32_16x16x128_f8f6f4 v[130:133], v[162:169], v[204:211], v[130:133], v185, v185 op_sel_hi:[0,0,0]
	s_nop 0
	s_add_i32 s68, s68, 2
	s_cmp_gt_u32 s68, 5
	s_barrier
; #define LAS __attribute__((address_space(3)))
;     __device__ __forceinline__ void operator()(g8::Acc& acc, const g8::Unit& u, int wr, int wc, int fr, int fq) const {
;         const int row0 = u.pm * 256 + wr * 64 + fr;
;         if (u.aux == 0) {
;             const LAS float* rp = rs + (u.flags >> 8) * 256 + wr * 64 + fr;
; #pragma unroll
;             for (int ai = 0; ai < 2; ++ai)
; #pragma unroll
;                 for (int m = 0; m < 4; ++m) { const float r = rp[ai * 128 + m * 16];
; #pragma unroll
;                     for (int bj = 0; bj < 2; ++bj)
; #pragma unroll
;                         for (int n = 0; n < 2; ++n) acc[ai][bj][m][n] *= r; }
;             return;
;         }
;         const int col0 = u.pn * 256 + wc * 32 + 8 * fq;
;         const int b = (u.pm * 256) >> 11;
;         f32x4 gt[2][2];
; #pragma unroll
;         for (int bj = 0; bj < 2; ++bj)
; #pragma unroll
;             for (int n = 0; n < 2; ++n) gt[bj][n] = *(const f32x4*)(mod + (size_t)b * NMOD + 2 * DM + col0 + bj * 128 + n * 4) * (1.0f / (CAT_SCALE * WOUT_SCALE));
; #pragma unroll
;         for (int am = 0; am < 4; ++am) {
;             const int ai = am >> 1, m0 = (am & 1) * 2;
;             f32x4 xv[2][2][2];
; #pragma unroll
;             for (int mm = 0; mm < 2; ++mm)
; #pragma unroll
;                 for (int bj = 0; bj < 2; ++bj) { const size_t off = (size_t)(row0 + ai * 128 + (m0 + mm) * 16) * DM + col0 + bj * 128; xv[mm][bj][0] = *(const f32x4*)(x + off); xv[mm][bj][1] = *(const f32x4*)(x + off + 4); }
; #pragma unroll
;             for (int mm = 0; mm < 2; ++mm) { const int m = m0 + mm; const int row = row0 + ai * 128 + m * 16; float ss = 0.f;
; #pragma unroll
;                 for (int bj = 0; bj < 2; ++bj) { const size_t off = (size_t)row * DM + col0 + bj * 128;
;                     const f32x4 o0 = xv[mm][bj][0] + gt[bj][0] * acc[ai][bj][m][0], o1 = xv[mm][bj][1] + gt[bj][1] * acc[ai][bj][m][1];
;                     ss += (o0[0] * o0[0] + o0[1] * o0[1]) + (o0[2] * o0[2] + o0[3] * o0[3]) + (o1[0] * o1[0] + o1[1] * o1[1]) + (o1[2] * o1[2] + o1[3] * o1[3]);
;                     u32x4 w; w.x = cvt_pk_bf16(o0[0], o0[1]); w.y = cvt_pk_bf16(o0[2], o0[3]); w.z = cvt_pk_bf16(o1[0], o1[1]); w.w = cvt_pk_bf16(o1[2], o1[3]);
;                     *(u32x4*)(X1 + off) = w; }
;                 ss += __shfl_xor(ss, 16); ss += __shfl_xor(ss, 32);
	s_cbranch_scc0 .LBB0_741
	s_mov_b32 s0, 0
	s_cmp_lg_u32 s4, 0
	v_mbcnt_lo_u32_b32 v2, -1, s0
	v_mbcnt_hi_u32_b32 v154, -1, v2
	v_and_b32_e32 v2, 15, v154
	s_cbranch_scc0 .LBB0_764
	s_lshl_b32 s0, s63, 8
	s_add_i32 s0, s0, s46
	v_or_b32_e32 v170, s0, v2
	s_lshl_b32 s0, s62, 8
	v_lshrrev_b32_e32 v4, 1, v154
	v_and_b32_e32 v4, 0x7ffffff8, v4
	s_or_b32 s0, s0, s47
	v_add_u32_e32 v4, s0, v4
	s_ashr_i32 s0, s63, 3
	s_mul_hi_i32 s1, s0, 0xc000
	s_mul_i32 s0, s0, 0xc000
	v_readlane_b32 s36, v254, 39
	v_readlane_b32 s37, v254, 40
	s_add_u32 s0, s36, s0
	v_ashrrev_i32_e32 v5, 31, v4
	s_addc_u32 s1, s37, s1
	v_lshlrev_b64 v[134:135], 2, v[4:5]
	v_lshl_add_u64 v[136:137], s[0:1], 0, v[134:135]
	v_lshl_add_u64 v[138:139], v[136:137], 0, s[24:25]
	v_add_co_u32_e32 v136, vcc, s53, v136
	v_readlane_b32 s64, v254, 7
	s_nop 0
	v_addc_co_u32_e32 v137, vcc, 0, v137, vcc
	v_readlane_b32 s65, v254, 8
	v_ashrrev_i32_e32 v171, 31, v170
	global_load_dwordx4 v[156:159], v[136:137], off
	global_load_dwordx4 v[190:193], v[138:139], off offset:528
	global_load_dwordx4 v[160:163], v[138:139], off offset:16
	global_load_dwordx4 v[194:197], v[138:139], off offset:512
	v_lshl_add_u64 v[172:173], s[64:65], 0, v[134:135]
	v_lshlrev_b64 v[134:135], 13, v[170:171]
	v_lshl_add_u64 v[134:135], v[172:173], 0, v[134:135]
	global_load_dwordx4 v[198:201], v[134:135], off
	global_load_dwordx4 v[202:205], v[134:135], off offset:16
	global_load_dwordx4 v[206:209], v[134:135], off offset:512
	global_load_dwordx4 v[210:213], v[134:135], off offset:528
	v_or_b32_e32 v174, 16, v170
	v_ashrrev_i32_e32 v175, 31, v174
	v_lshlrev_b64 v[134:135], 13, v[174:175]
	v_lshl_add_u64 v[138:139], v[172:173], 0, v[134:135]
	global_load_dwordx4 v[142:145], v[138:139], off offset:16
	global_load_dwordx4 v[146:149], v[138:139], off
	global_load_dwordx4 v[134:137], v[138:139], off offset:528
	s_nop 0
	global_load_dwordx4 v[138:141], v[138:139], off offset:512
	v_and_b32_e32 v164, 64, v186
	v_xor_b32_e32 v155, 16, v186
	v_cmp_gt_u32_e32 vcc, 16, v154
	v_add_u32_e32 v154, 64, v164
	v_xor_b32_e32 v165, 32, v186
	v_cmp_lt_i32_e64 s[0:1], v155, v154
	v_lshlrev_b64 v[176:177], 12, v[170:171]
	v_lshl_add_u64 v[176:177], s[12:13], 0, v[176:177]
	v_cndmask_b32_e64 v155, v186, v155, s[0:1]
	v_cmp_lt_i32_e64 s[0:1], v165, v154
	v_lshlrev_b32_e32 v188, 2, v155
	v_readlane_b32 s38, v254, 41
	v_cndmask_b32_e64 v154, v186, v165, s[0:1]
	v_lshlrev_b32_e32 v187, 2, v154
	v_readlane_b32 s39, v254, 42
	v_readlane_b32 s66, v254, 9
	v_readlane_b32 s67, v254, 10
	v_readlane_b32 s68, v254, 11
	v_readlane_b32 s69, v254, 12
	v_readlane_b32 s70, v254, 13
	v_readlane_b32 s71, v254, 14
	v_readlane_b32 s72, v254, 15
	v_readlane_b32 s73, v254, 16
	v_readlane_b32 s74, v254, 17
	v_readlane_b32 s75, v254, 18
	v_readlane_b32 s76, v254, 19
	v_readlane_b32 s77, v254, 20
	v_readlane_b32 s78, v254, 21
	v_readlane_b32 s79, v254, 22
	v_or_b32_e32 v216, 32, v170
	v_ashrrev_i32_e32 v217, 31, v216
	v_lshlrev_b64 v[214:215], 13, v[216:217]
	v_lshl_add_u64 v[214:215], v[172:173], 0, v[214:215]
	global_load_dwordx4 v[230:233], v[214:215], off
	global_load_dwordx4 v[234:237], v[214:215], off offset:16
	global_load_dwordx4 v[238:241], v[214:215], off offset:512
	global_load_dwordx4 v[242:245], v[214:215], off offset:528
	v_or_b32_e32 v216, 48, v170
	v_ashrrev_i32_e32 v217, 31, v216
	v_lshlrev_b64 v[214:215], 13, v[216:217]
	v_lshl_add_u64 v[218:219], v[172:173], 0, v[214:215]
	global_load_dwordx4 v[222:225], v[218:219], off offset:16
	global_load_dwordx4 v[226:229], v[218:219], off
	global_load_dwordx4 v[214:217], v[218:219], off offset:528
	s_nop 0
	global_load_dwordx4 v[218:221], v[218:219], off offset:512
	s_waitcnt vmcnt(8)
	v_pk_mul_f32 v[166:167], v[158:159], s[26:27] op_sel_hi:[1,0]
	v_pk_mul_f32 v[168:169], v[156:157], s[26:27] op_sel_hi:[1,0]
	v_pk_mul_f32 v[164:165], v[162:163], s[26:27] op_sel_hi:[1,0]
	v_pk_mul_f32 v[162:163], v[160:161], s[26:27] op_sel_hi:[1,0]
	v_pk_mul_f32 v[158:159], v[196:197], s[26:27] op_sel_hi:[1,0]
	v_pk_mul_f32 v[160:161], v[194:195], s[26:27] op_sel_hi:[1,0]
	v_pk_mul_f32 v[154:155], v[190:191], s[26:27] op_sel_hi:[1,0]
	v_pk_fma_f32 v[194:195], v[8:9], v[166:167], v[200:201]
	v_pk_fma_f32 v[196:197], v[6:7], v[168:169], v[198:199]
	v_pk_fma_f32 v[198:199], v[12:13], v[164:165], v[204:205]
	v_pk_fma_f32 v[200:201], v[10:11], v[162:163], v[202:203]
	v_pk_fma_f32 v[202:203], v[40:41], v[158:159], v[208:209]
	v_pk_fma_f32 v[204:205], v[38:39], v[160:161], v[206:207]
	v_pk_mul_f32 v[156:157], v[192:193], s[26:27] op_sel_hi:[1,0]
	v_pk_fma_f32 v[208:209], v[42:43], v[154:155], v[210:211]
	v_mul_f32_e32 v189, v197, v197
	v_mul_f32_e32 v210, v195, v195
	v_cvt_pk_bf16_f32 v190, v196, v197
	v_cvt_pk_bf16_f32 v191, v194, v195
	v_mul_f32_e32 v195, v205, v205
	v_mul_f32_e32 v197, v203, v203
	v_pk_fma_f32 v[206:207], v[44:45], v[156:157], v[212:213]
	v_mul_f32_e32 v211, v201, v201
	v_mul_f32_e32 v212, v199, v199
	v_cvt_pk_bf16_f32 v193, v198, v199
	v_mul_f32_e32 v199, v209, v209
	v_fmac_f32_e32 v189, v196, v196
	v_fmac_f32_e32 v210, v194, v194
	v_fmac_f32_e32 v195, v204, v204
	v_fmac_f32_e32 v197, v202, v202
	v_cvt_pk_bf16_f32 v192, v200, v201
	v_mul_f32_e32 v201, v207, v207
	v_fmac_f32_e32 v211, v200, v200
	v_fmac_f32_e32 v199, v208, v208
	v_add_f32_e32 v189, v189, v210
	v_add_f32_e32 v194, v195, v197
	v_fmac_f32_e32 v212, v198, v198
	v_fmac_f32_e32 v201, v206, v206
	v_add_f32_e32 v189, v189, v211
	v_add_f32_e32 v194, v194, v199
	v_add_f32_e32 v189, v212, v189
	v_add_f32_e32 v194, v201, v194
	v_add_f32_e32 v189, v189, v194
	ds_bpermute_b32 v196, v188, v189
	v_lshl_add_u64 v[194:195], v[4:5], 1, v[176:177]
	global_store_dwordx4 v[194:195], v[190:193], off
	s_waitcnt lgkmcnt(0)
	v_add_f32_e32 v176, v189, v196
	ds_bpermute_b32 v177, v187, v176
	v_cvt_pk_bf16_f32 v190, v204, v205
	v_cvt_pk_bf16_f32 v191, v202, v203
	v_cvt_pk_bf16_f32 v192, v208, v209
	v_cvt_pk_bf16_f32 v193, v206, v207
	global_store_dwordx4 v[194:195], v[190:193], off offset:256
	s_and_saveexec_b64 s[0:1], vcc
	s_cbranch_execz .LBB0_745
	s_waitcnt lgkmcnt(0)
	v_add_f32_e32 v189, v176, v177
	s_lshl_b32 s34, s62, 2
	v_lshlrev_b64 v[176:177], 7, v[170:171]
	s_ashr_i32 s35, s34, 31
	v_lshl_add_u64 v[176:177], s[10:11], 0, v[176:177]
	v_lshl_add_u64 v[176:177], s[34:35], 2, v[176:177]
	s_lshl_b32 s4, s45, 2
	v_lshl_add_u64 v[176:177], v[176:177], 0, s[4:5]
	global_store_dword v[176:177], v189, off

; #define G8_STAGE(bufoff, gbase, v0, v1) do { unsigned x0_ = (v0), x1_ = (v1); asm volatile("" : "+v"(x0_), "+v"(x1_));     \
;         __builtin_amdgcn_global_load_lds((const unsigned*)((gbase) + x0_), (LAS unsigned*)(lds + (bufoff) + ldsw), 16, 0, 0); \
;         __builtin_amdgcn_global_load_lds((const unsigned*)((gbase) + x1_), (LAS unsigned*)(lds + (bufoff) + ldsw + 8192), 16, 0, 0); } while (0)
; #define G8_LDA(dst, b, h) do { _Pragma("unroll") for (int m = 0; m < 4; ++m) _Pragma("unroll") for (int k = 0; k < 2; ++k) dst[m][k] = *(const LAS bf16x8*)(lds + G8_SA(b, h) + aoff + m * 2048 + k * 1024); } while (0)
; #define G8_LDB(dst, b, h) do { _Pragma("unroll") for (int n = 0; n < 2; ++n) _Pragma("unroll") for (int k = 0; k < 2; ++k) dst[n][k] = *(const LAS bf16x8*)(lds + G8_SB(b, h) + boff + n * 2048 + k * 1024); } while (0)
; #define G8_WAIT_L(n) asm volatile("s_waitcnt lgkmcnt(" #n ")" ::: "memory")
; #define G8_BAR __builtin_amdgcn_s_barrier()
; #define G8_SCHED __builtin_amdgcn_sched_barrier(0)
;     ...
;             G8_LDB(B0, 0, 0); G8_SCHED; G8_LDA(At, 0, 0); G8_STAGE(G8_SA(1, 1), a1, cv[1][0], cv[1][1]);
;             G8_WAIT_L(8); G8_BAR; G8_WAIT_L(0); if (do0) G8_MMA(0, 0, At, B0); G8_CONV_CVT; G8_BAR; G8_SCHED;
;             G8_LDB(B1, 0, 1); G8_STAGE(G8_SB(0, 0), b2, voffB[0], voffB[1]);
;             G8_BAR; G8_CONV_ISSUE;
;             G8_WAIT_L(0); if (do0) G8_MMA(0, 1, At, B1); G8_BAR;
;             G8_LDA(At, 0, 1); G8_STAGE(G8_SA(0, 0), a2, o00, o01);
;             G8_BAR; G8_WAIT_L(0); if (do1) G8_MMA(1, 0, At, B0); G8_BAR; G8_SCHED;
.LBB0_1156:
	s_add_u32 s4, s38, 0x80
	s_addc_u32 s5, s39, 0
	s_add_u32 s48, s38, 0x100
	s_addc_u32 s49, s39, 0
	s_add_u32 s87, s40, 0x10000
	s_addc_u32 s88, s41, 0
	s_cmp_eq_u32 s86, 12
	s_cselect_b64 s[8:9], -1, 0
	s_and_b64 s[6:7], s[8:9], exec
	s_cselect_b32 s51, s43, s49
	s_cselect_b32 s50, s42, s48
	s_cselect_b32 s49, s84, s88
	s_cselect_b32 s48, s85, s87
	v_add_u32_e32 v14, 0x10000, v210
	ds_read_b128 v[2:5], v14
	ds_read_b128 v[6:9], v14 offset:1024
	ds_read_b128 v[10:13], v14 offset:2048
	ds_read_b128 v[14:17], v14 offset:3072
	v_mov_b32_e32 v18, v218
	v_mov_b32_e32 v19, v219
	s_add_i32 m0, s54, 0xc000
	s_waitcnt lgkmcnt(0)
	ds_read_b128 v[58:61], v211
	ds_read_b128 v[62:65], v211 offset:1024
	ds_read_b128 v[50:53], v211 offset:2048
	ds_read_b128 v[54:57], v211 offset:3072
	ds_read_b128 v[42:45], v211 offset:4096
	ds_read_b128 v[46:49], v211 offset:5120
	ds_read_b128 v[34:37], v211 offset:6144
	ds_read_b128 v[38:41], v211 offset:7168
	s_andn2_b64 vcc, exec, s[44:45]
	global_load_lds_dwordx4 v18, s[4:5]
	s_add_i32 m0, s54, 0xe000
	v_cndmask_b32_e64 v18, 0, 1, s[44:45]
	global_load_lds_dwordx4 v19, s[4:5]
	s_waitcnt lgkmcnt(8)
	s_barrier
	s_waitcnt lgkmcnt(0)
	v_cmp_ne_u32_e64 s[6:7], 1, v18
	s_cbranch_vccnz .LBB0_1158
	s_nop 0
	s_waitcnt lgkmcnt(0)
	v_mfma_scale_f32_16x16x128_f8f6f4 v[98:101], v[2:9], v[58:65], v[98:101], v209, v209 op_sel_hi:[0,0,0]
	v_mfma_scale_f32_16x16x128_f8f6f4 v[94:97], v[10:17], v[58:65], v[94:97], v209, v209 op_sel_hi:[0,0,0]
	v_mfma_scale_f32_16x16x128_f8f6f4 v[90:93], v[2:9], v[50:57], v[90:93], v209, v209 op_sel_hi:[0,0,0]
	v_mfma_scale_f32_16x16x128_f8f6f4 v[86:89], v[10:17], v[50:57], v[86:89], v209, v209 op_sel_hi:[0,0,0]
	v_mfma_scale_f32_16x16x128_f8f6f4 v[82:85], v[2:9], v[42:49], v[82:85], v209, v209 op_sel_hi:[0,0,0]
	v_mfma_scale_f32_16x16x128_f8f6f4 v[78:81], v[10:17], v[42:49], v[78:81], v209, v209 op_sel_hi:[0,0,0]
	v_mfma_scale_f32_16x16x128_f8f6f4 v[74:77], v[2:9], v[34:41], v[74:77], v209, v209 op_sel_hi:[0,0,0]
	v_mfma_scale_f32_16x16x128_f8f6f4 v[70:73], v[10:17], v[34:41], v[70:73], v209, v209 op_sel_hi:[0,0,0]
	s_nop 0
.LBB0_1158:
	s_barrier
	s_mov_b32 m0, s55
	v_add_u32_e32 v30, 0x14000, v210
	v_mov_b32_e32 v66, v208
	v_mov_b32_e32 v68, v207
	ds_read_b128 v[18:21], v30
	ds_read_b128 v[22:25], v30 offset:1024
	ds_read_b128 v[26:29], v30 offset:2048
	ds_read_b128 v[30:33], v30 offset:3072
	s_and_b64 vcc, exec, s[6:7]
	global_load_lds_dwordx4 v68, s[48:49]
	s_mov_b32 m0, s56
	s_nop 0
	global_load_lds_dwordx4 v66, s[48:49]
	s_barrier
	s_waitcnt lgkmcnt(0)
	s_cbranch_vccnz .LBB0_1160
	s_nop 0
	s_waitcnt lgkmcnt(0)
	v_mfma_scale_f32_16x16x128_f8f6f4 v[130:133], v[18:25], v[58:65], v[130:133], v209, v209 op_sel_hi:[0,0,0]
	v_mfma_scale_f32_16x16x128_f8f6f4 v[126:129], v[26:33], v[58:65], v[126:129], v209, v209 op_sel_hi:[0,0,0]
	v_mfma_scale_f32_16x16x128_f8f6f4 v[122:125], v[18:25], v[50:57], v[122:125], v209, v209 op_sel_hi:[0,0,0]
	v_mfma_scale_f32_16x16x128_f8f6f4 v[118:121], v[26:33], v[50:57], v[118:121], v209, v209 op_sel_hi:[0,0,0]
	v_mfma_scale_f32_16x16x128_f8f6f4 v[114:117], v[18:25], v[42:49], v[114:117], v209, v209 op_sel_hi:[0,0,0]
	v_mfma_scale_f32_16x16x128_f8f6f4 v[110:113], v[26:33], v[42:49], v[110:113], v209, v209 op_sel_hi:[0,0,0]
	v_mfma_scale_f32_16x16x128_f8f6f4 v[106:109], v[18:25], v[34:41], v[106:109], v209, v209 op_sel_hi:[0,0,0]
	v_mfma_scale_f32_16x16x128_f8f6f4 v[102:105], v[26:33], v[34:41], v[102:105], v209, v209 op_sel_hi:[0,0,0]
	s_nop 0
.LBB0_1160:
	v_cndmask_b32_e64 v66, v216, v212, s[8:9]
	v_cndmask_b32_e64 v68, v217, v213, s[8:9]
	s_mov_b32 m0, s54
	v_mov_b32_e32 v69, v66
	v_mov_b32_e32 v220, v68
	s_barrier
	s_waitcnt lgkmcnt(0)
	ds_read_b128 v[58:61], v211 offset:16384
	ds_read_b128 v[62:65], v211 offset:17408
	ds_read_b128 v[50:53], v211 offset:18432
	ds_read_b128 v[54:57], v211 offset:19456
	ds_read_b128 v[42:45], v211 offset:20480
	ds_read_b128 v[46:49], v211 offset:21504
	ds_read_b128 v[34:37], v211 offset:22528
	ds_read_b128 v[38:41], v211 offset:23552
	s_andn2_b64 vcc, exec, s[46:47]
	global_load_lds_dwordx4 v69, s[50:51]
	s_mov_b32 m0, s57
	v_cndmask_b32_e64 v69, 0, 1, s[46:47]
	global_load_lds_dwordx4 v220, s[50:51]
	s_barrier
	s_waitcnt lgkmcnt(0)
	v_cmp_ne_u32_e64 s[4:5], 1, v69
	s_cbranch_vccnz .LBB0_1162
	s_nop 0
	s_waitcnt lgkmcnt(0)
	v_mfma_scale_f32_16x16x128_f8f6f4 v[162:165], v[2:9], v[58:65], v[162:165], v209, v209 op_sel_hi:[0,0,0]
	v_mfma_scale_f32_16x16x128_f8f6f4 v[158:161], v[10:17], v[58:65], v[158:161], v209, v209 op_sel_hi:[0,0,0]
	v_mfma_scale_f32_16x16x128_f8f6f4 v[154:157], v[2:9], v[50:57], v[154:157], v209, v209 op_sel_hi:[0,0,0]
	v_mfma_scale_f32_16x16x128_f8f6f4 v[150:153], v[10:17], v[50:57], v[150:153], v209, v209 op_sel_hi:[0,0,0]
	v_mfma_scale_f32_16x16x128_f8f6f4 v[146:149], v[2:9], v[42:49], v[146:149], v209, v209 op_sel_hi:[0,0,0]
	v_mfma_scale_f32_16x16x128_f8f6f4 v[142:145], v[10:17], v[42:49], v[142:145], v209, v209 op_sel_hi:[0,0,0]
	v_mfma_scale_f32_16x16x128_f8f6f4 v[138:141], v[2:9], v[34:41], v[138:141], v209, v209 op_sel_hi:[0,0,0]
	v_mfma_scale_f32_16x16x128_f8f6f4 v[134:137], v[10:17], v[34:41], v[134:137], v209, v209 op_sel_hi:[0,0,0]
	s_nop 0
; #define G8_STAGE(bufoff, gbase, v0, v1) do { unsigned x0_ = (v0), x1_ = (v1); asm volatile("" : "+v"(x0_), "+v"(x1_));     \
;         __builtin_amdgcn_global_load_lds((const unsigned*)((gbase) + x0_), (LAS unsigned*)(lds + (bufoff) + ldsw), 16, 0, 0); \
;         __builtin_amdgcn_global_load_lds((const unsigned*)((gbase) + x1_), (LAS unsigned*)(lds + (bufoff) + ldsw + 8192), 16, 0, 0); } while (0)
; #define G8_LDA(dst, b, h) do { _Pragma("unroll") for (int m = 0; m < 4; ++m) _Pragma("unroll") for (int k = 0; k < 2; ++k) dst[m][k] = *(const LAS bf16x8*)(lds + G8_SA(b, h) + aoff + m * 2048 + k * 1024); } while (0)
; #define G8_LDB(dst, b, h) do { _Pragma("unroll") for (int n = 0; n < 2; ++n) _Pragma("unroll") for (int k = 0; k < 2; ++k) dst[n][k] = *(const LAS bf16x8*)(lds + G8_SB(b, h) + boff + n * 2048 + k * 1024); } while (0)
; #define G8_WAIT_V(n) asm volatile("s_waitcnt vmcnt(" #n ")" ::: "memory")
; #define G8_WAIT_L(n) asm volatile("s_waitcnt lgkmcnt(" #n ")" ::: "memory")
; #define G8_BAR __builtin_amdgcn_s_barrier()
; #define G8_SCHED __builtin_amdgcn_sched_barrier(0)
;     ...
;             G8_STAGE(G8_SB(0, 1), b2 + hstepB, voffB[0], voffB[1]);
;             if constexpr (CONV) G8_WAIT_V(9); else G8_WAIT_V(6);
;             G8_BAR; if (do1) G8_MMA(1, 1, At, B1); G8_BAR;
;             G8_LDB(B0, 1, 0); G8_SCHED; G8_LDA(At, 1, 0); G8_STAGE(G8_SA(0, 1), a2, o10, o11);
;             G8_WAIT_L(8); G8_BAR; G8_WAIT_L(0); if (do0) G8_MMA(0, 0, At, B0); G8_BAR; G8_SCHED;
.LBB0_1162:
	s_barrier
	s_add_u32 s88, s48, 0x4000
	s_mov_b32 m0, s58
	v_mov_b32_e32 v2, v207
	v_mov_b32_e32 v3, v208
	s_addc_u32 s89, s49, 0
	s_and_b64 vcc, exec, s[4:5]
	global_load_lds_dwordx4 v2, s[88:89]
	s_mov_b32 m0, s59
	s_nop 0
	global_load_lds_dwordx4 v3, s[88:89]
	s_waitcnt vmcnt(6)
	s_barrier
	s_cbranch_vccnz .LBB0_1164
	s_nop 0
	s_waitcnt lgkmcnt(0)
	v_mfma_scale_f32_16x16x128_f8f6f4 v[194:197], v[18:25], v[58:65], v[194:197], v209, v209 op_sel_hi:[0,0,0]
	v_mfma_scale_f32_16x16x128_f8f6f4 v[190:193], v[26:33], v[58:65], v[190:193], v209, v209 op_sel_hi:[0,0,0]
	v_mfma_scale_f32_16x16x128_f8f6f4 v[186:189], v[18:25], v[50:57], v[186:189], v209, v209 op_sel_hi:[0,0,0]
	v_mfma_scale_f32_16x16x128_f8f6f4 v[182:185], v[26:33], v[50:57], v[182:185], v209, v209 op_sel_hi:[0,0,0]
	v_mfma_scale_f32_16x16x128_f8f6f4 v[178:181], v[18:25], v[42:49], v[178:181], v209, v209 op_sel_hi:[0,0,0]
	v_mfma_scale_f32_16x16x128_f8f6f4 v[174:177], v[26:33], v[42:49], v[174:177], v209, v209 op_sel_hi:[0,0,0]
	v_mfma_scale_f32_16x16x128_f8f6f4 v[170:173], v[18:25], v[34:41], v[170:173], v209, v209 op_sel_hi:[0,0,0]
	v_mfma_scale_f32_16x16x128_f8f6f4 v[166:169], v[26:33], v[34:41], v[166:169], v209, v209 op_sel_hi:[0,0,0]
	s_nop 0
.LBB0_1164:
	v_add_u32_e32 v14, 0x18000, v210
	s_barrier
	ds_read_b128 v[2:5], v14
	ds_read_b128 v[6:9], v14 offset:1024
	ds_read_b128 v[10:13], v14 offset:2048
	ds_read_b128 v[14:17], v14 offset:3072
	v_cndmask_b32_e64 v18, v218, v214, s[8:9]
	v_cndmask_b32_e64 v19, v219, v215, s[8:9]
	s_mov_b32 m0, s60
	s_waitcnt lgkmcnt(0)
	ds_read_b128 v[58:61], v211 offset:32768
	ds_read_b128 v[62:65], v211 offset:33792
	ds_read_b128 v[50:53], v211 offset:34816
	ds_read_b128 v[54:57], v211 offset:35840
	ds_read_b128 v[42:45], v211 offset:36864
	ds_read_b128 v[46:49], v211 offset:37888
	ds_read_b128 v[34:37], v211 offset:38912
	ds_read_b128 v[38:41], v211 offset:39936
	s_and_b64 vcc, exec, s[6:7]
	global_load_lds_dwordx4 v18, s[50:51]
	s_mov_b32 m0, s61
	s_nop 0
	global_load_lds_dwordx4 v19, s[50:51]
	s_waitcnt lgkmcnt(8)
	s_barrier
	s_waitcnt lgkmcnt(0)
	s_cbranch_vccnz .LBB0_1166
	s_nop 0
	s_waitcnt lgkmcnt(0)
	v_mfma_scale_f32_16x16x128_f8f6f4 v[98:101], v[2:9], v[58:65], v[98:101], v209, v209 op_sel_hi:[0,0,0]
	v_mfma_scale_f32_16x16x128_f8f6f4 v[94:97], v[10:17], v[58:65], v[94:97], v209, v209 op_sel_hi:[0,0,0]
	v_mfma_scale_f32_16x16x128_f8f6f4 v[90:93], v[2:9], v[50:57], v[90:93], v209, v209 op_sel_hi:[0,0,0]
	v_mfma_scale_f32_16x16x128_f8f6f4 v[86:89], v[10:17], v[50:57], v[86:89], v209, v209 op_sel_hi:[0,0,0]
	v_mfma_scale_f32_16x16x128_f8f6f4 v[82:85], v[2:9], v[42:49], v[82:85], v209, v209 op_sel_hi:[0,0,0]
	v_mfma_scale_f32_16x16x128_f8f6f4 v[78:81], v[10:17], v[42:49], v[78:81], v209, v209 op_sel_hi:[0,0,0]
	v_mfma_scale_f32_16x16x128_f8f6f4 v[74:77], v[2:9], v[34:41], v[74:77], v209, v209 op_sel_hi:[0,0,0]
	v_mfma_scale_f32_16x16x128_f8f6f4 v[70:73], v[10:17], v[34:41], v[70:73], v209, v209 op_sel_hi:[0,0,0]
	s_nop 0
; #define G8_STAGE(bufoff, gbase, v0, v1) do { unsigned x0_ = (v0), x1_ = (v1); asm volatile("" : "+v"(x0_), "+v"(x1_));     \
;         __builtin_amdgcn_global_load_lds((const unsigned*)((gbase) + x0_), (LAS unsigned*)(lds + (bufoff) + ldsw), 16, 0, 0); \
;         __builtin_amdgcn_global_load_lds((const unsigned*)((gbase) + x1_), (LAS unsigned*)(lds + (bufoff) + ldsw + 8192), 16, 0, 0); } while (0)
; #define G8_LDA(dst, b, h) do { _Pragma("unroll") for (int m = 0; m < 4; ++m) _Pragma("unroll") for (int k = 0; k < 2; ++k) dst[m][k] = *(const LAS bf16x8*)(lds + G8_SA(b, h) + aoff + m * 2048 + k * 1024); } while (0)
; #define G8_LDB(dst, b, h) do { _Pragma("unroll") for (int n = 0; n < 2; ++n) _Pragma("unroll") for (int k = 0; k < 2; ++k) dst[n][k] = *(const LAS bf16x8*)(lds + G8_SB(b, h) + boff + n * 2048 + k * 1024); } while (0)
; #define G8_WAIT_V(n) asm volatile("s_waitcnt vmcnt(" #n ")" ::: "memory")
; #define G8_WAIT_L(n) asm volatile("s_waitcnt lgkmcnt(" #n ")" ::: "memory")
; #define G8_BAR __builtin_amdgcn_s_barrier()
; #define G8_SCHED __builtin_amdgcn_sched_barrier(0)
;     ...
;             G8_LDB(B1, 1, 1); G8_STAGE(G8_SB(1, 0), b3, voffB[0], voffB[1]);
;             G8_BAR; G8_WAIT_L(0); if (do0) G8_MMA(0, 1, At, B1); G8_BAR;
;             G8_LDA(At, 1, 1); G8_STAGE(G8_SA(1, 0), a3, o00, o01);
;             G8_BAR; G8_WAIT_L(0); if (do1) G8_MMA(1, 0, At, B0); G8_BAR; G8_SCHED;
;             G8_STAGE(G8_SB(1, 1), b3 + hstepB, voffB[0], voffB[1]);
;             G8_WAIT_V(6); G8_BAR; if (do1) G8_MMA(1, 1, At, B1); G8_BAR;
.LBB0_1166:
	s_add_u32 s8, s48, 0x8000
	s_addc_u32 s9, s49, 0
	s_barrier
	s_mov_b32 m0, s64
	v_add_u32_e32 v30, 0x1c000, v210
	v_mov_b32_e32 v69, v208
	v_mov_b32_e32 v220, v207
	ds_read_b128 v[18:21], v30
	ds_read_b128 v[22:25], v30 offset:1024
	ds_read_b128 v[26:29], v30 offset:2048
	ds_read_b128 v[30:33], v30 offset:3072
	s_and_b64 vcc, exec, s[6:7]
	global_load_lds_dwordx4 v220, s[8:9]
	s_mov_b32 m0, s65
	s_nop 0
	global_load_lds_dwordx4 v69, s[8:9]
	s_barrier
	s_waitcnt lgkmcnt(0)
	s_cbranch_vccnz .LBB0_1168
	s_nop 0
	s_waitcnt lgkmcnt(0)
	v_mfma_scale_f32_16x16x128_f8f6f4 v[130:133], v[18:25], v[58:65], v[130:133], v209, v209 op_sel_hi:[0,0,0]
	v_mfma_scale_f32_16x16x128_f8f6f4 v[126:129], v[26:33], v[58:65], v[126:129], v209, v209 op_sel_hi:[0,0,0]
	v_mfma_scale_f32_16x16x128_f8f6f4 v[122:125], v[18:25], v[50:57], v[122:125], v209, v209 op_sel_hi:[0,0,0]
	v_mfma_scale_f32_16x16x128_f8f6f4 v[118:121], v[26:33], v[50:57], v[118:121], v209, v209 op_sel_hi:[0,0,0]
	v_mfma_scale_f32_16x16x128_f8f6f4 v[114:117], v[18:25], v[42:49], v[114:117], v209, v209 op_sel_hi:[0,0,0]
	v_mfma_scale_f32_16x16x128_f8f6f4 v[110:113], v[26:33], v[42:49], v[110:113], v209, v209 op_sel_hi:[0,0,0]
	v_mfma_scale_f32_16x16x128_f8f6f4 v[106:109], v[18:25], v[34:41], v[106:109], v209, v209 op_sel_hi:[0,0,0]
	v_mfma_scale_f32_16x16x128_f8f6f4 v[102:105], v[26:33], v[34:41], v[102:105], v209, v209 op_sel_hi:[0,0,0]
	s_nop 0
.LBB0_1168:
	s_barrier
	s_waitcnt lgkmcnt(0)
	ds_read_b128 v[58:61], v211 offset:49152
	ds_read_b128 v[62:65], v211 offset:50176
	ds_read_b128 v[50:53], v211 offset:51200
	ds_read_b128 v[54:57], v211 offset:52224
	ds_read_b128 v[42:45], v211 offset:53248
	ds_read_b128 v[46:49], v211 offset:54272
	ds_read_b128 v[34:37], v211 offset:55296
	ds_read_b128 v[38:41], v211 offset:56320
	v_mov_b32_e32 v69, v67
	v_lshl_add_u64 v[220:221], s[50:51], 0, v[66:67]
	s_mov_b32 m0, s66
	v_lshl_add_u64 v[220:221], v[220:221], 0, s[24:25]
	v_lshl_add_u64 v[68:69], s[50:51], 0, v[68:69]
	global_load_lds_dwordx4 v[220:221], off
	v_lshl_add_u64 v[68:69], v[68:69], 0, s[24:25]
	s_mov_b32 m0, s67
	s_and_b64 vcc, exec, s[4:5]
	global_load_lds_dwordx4 v[68:69], off
	s_barrier
	s_waitcnt lgkmcnt(0)
	s_cbranch_vccnz .LBB0_1170
	s_nop 0
	s_waitcnt lgkmcnt(0)
	v_mfma_scale_f32_16x16x128_f8f6f4 v[162:165], v[2:9], v[58:65], v[162:165], v209, v209 op_sel_hi:[0,0,0]
	v_mfma_scale_f32_16x16x128_f8f6f4 v[158:161], v[10:17], v[58:65], v[158:161], v209, v209 op_sel_hi:[0,0,0]
	v_mfma_scale_f32_16x16x128_f8f6f4 v[154:157], v[2:9], v[50:57], v[154:157], v209, v209 op_sel_hi:[0,0,0]
	v_mfma_scale_f32_16x16x128_f8f6f4 v[150:153], v[10:17], v[50:57], v[150:153], v209, v209 op_sel_hi:[0,0,0]
	v_mfma_scale_f32_16x16x128_f8f6f4 v[146:149], v[2:9], v[42:49], v[146:149], v209, v209 op_sel_hi:[0,0,0]
	v_mfma_scale_f32_16x16x128_f8f6f4 v[142:145], v[10:17], v[42:49], v[142:145], v209, v209 op_sel_hi:[0,0,0]
	v_mfma_scale_f32_16x16x128_f8f6f4 v[138:141], v[2:9], v[34:41], v[138:141], v209, v209 op_sel_hi:[0,0,0]
	v_mfma_scale_f32_16x16x128_f8f6f4 v[134:137], v[10:17], v[34:41], v[134:137], v209, v209 op_sel_hi:[0,0,0]
	s_nop 0
.LBB0_1170:
	s_barrier
	s_add_u32 s6, s48, 0xc000
	s_mov_b32 m0, s68
	v_mov_b32_e32 v2, v207
	v_mov_b32_e32 v3, v208
	s_addc_u32 s7, s49, 0
	s_and_b64 vcc, exec, s[4:5]
	global_load_lds_dwordx4 v2, s[6:7]
	s_mov_b32 m0, s69
	s_nop 0
	global_load_lds_dwordx4 v3, s[6:7]
	s_waitcnt vmcnt(6)
	s_barrier
	s_cbranch_vccnz .LBB0_1155
	s_nop 0
	s_waitcnt lgkmcnt(0)
	v_mfma_scale_f32_16x16x128_f8f6f4 v[194:197], v[18:25], v[58:65], v[194:197], v209, v209 op_sel_hi:[0,0,0]
	v_mfma_scale_f32_16x16x128_f8f6f4 v[190:193], v[26:33], v[58:65], v[190:193], v209, v209 op_sel_hi:[0,0,0]
	v_mfma_scale_f32_16x16x128_f8f6f4 v[186:189], v[18:25], v[50:57], v[186:189], v209, v209 op_sel_hi:[0,0,0]
	v_mfma_scale_f32_16x16x128_f8f6f4 v[182:185], v[26:33], v[50:57], v[182:185], v209, v209 op_sel_hi:[0,0,0]
	v_mfma_scale_f32_16x16x128_f8f6f4 v[178:181], v[18:25], v[42:49], v[178:181], v209, v209 op_sel_hi:[0,0,0]
	v_mfma_scale_f32_16x16x128_f8f6f4 v[174:177], v[26:33], v[42:49], v[174:177], v209, v209 op_sel_hi:[0,0,0]
	v_mfma_scale_f32_16x16x128_f8f6f4 v[170:173], v[18:25], v[34:41], v[170:173], v209, v209 op_sel_hi:[0,0,0]
	v_mfma_scale_f32_16x16x128_f8f6f4 v[166:169], v[26:33], v[34:41], v[166:169], v209, v209 op_sel_hi:[0,0,0]
	s_nop 0
	s_branch .LBB0_1155

; #define G8_STAGE(bufoff, gbase, v0, v1) do { unsigned x0_ = (v0), x1_ = (v1); asm volatile("" : "+v"(x0_), "+v"(x1_));     \
;         __builtin_amdgcn_global_load_lds((const unsigned*)((gbase) + x0_), (LAS unsigned*)(lds + (bufoff) + ldsw), 16, 0, 0); \
;         __builtin_amdgcn_global_load_lds((const unsigned*)((gbase) + x1_), (LAS unsigned*)(lds + (bufoff) + ldsw + 8192), 16, 0, 0); } while (0)
; #define G8_LDA(dst, b, h) do { _Pragma("unroll") for (int m = 0; m < 4; ++m) _Pragma("unroll") for (int k = 0; k < 2; ++k) dst[m][k] = *(const LAS bf16x8*)(lds + G8_SA(b, h) + aoff + m * 2048 + k * 1024); } while (0)
; #define G8_LDB(dst, b, h) do { _Pragma("unroll") for (int n = 0; n < 2; ++n) _Pragma("unroll") for (int k = 0; k < 2; ++k) dst[n][k] = *(const LAS bf16x8*)(lds + G8_SB(b, h) + boff + n * 2048 + k * 1024); } while (0)
; #define G8_WAIT_L(n) asm volatile("s_waitcnt lgkmcnt(" #n ")" ::: "memory")
; #define G8_BAR __builtin_amdgcn_s_barrier()
; #define G8_SCHED __builtin_amdgcn_sched_barrier(0)
;     ...
;             G8_LDB(B0, 0, 0); G8_SCHED; G8_LDA(At, 0, 0); G8_STAGE(G8_SA(1, 1), a1, cv[1][0], cv[1][1]);
;             G8_WAIT_L(8); G8_BAR; G8_WAIT_L(0); if (do0) G8_MMA(0, 0, At, B0); G8_CONV_CVT; G8_BAR; G8_SCHED;
;             G8_LDB(B1, 0, 1); G8_STAGE(G8_SB(0, 0), b2, voffB[0], voffB[1]);
;             G8_BAR; G8_CONV_ISSUE;
;             G8_WAIT_L(0); if (do0) G8_MMA(0, 1, At, B1); G8_BAR;
;             G8_LDA(At, 0, 1); G8_STAGE(G8_SA(0, 0), a2, o00, o01);
;             G8_BAR; G8_WAIT_L(0); if (do1) G8_MMA(1, 0, At, B0); G8_BAR; G8_SCHED;
.LBB0_1357:
	s_add_u32 s4, s26, 0x80
	s_addc_u32 s5, s27, 0
	s_add_u32 s6, s26, 0x100
	s_addc_u32 s7, s27, 0
	s_add_u32 s36, s28, 0x10000
	s_addc_u32 s37, s29, 0
	s_cmp_eq_u32 s75, 4
	s_cselect_b32 s39, s71, s7
	s_cselect_b32 s38, s72, s6
	s_cselect_b32 s37, s73, s37
	s_cselect_b32 s36, s74, s36
	v_add_u32_e32 v14, 0x10000, v204
	ds_read_b128 v[2:5], v14
	ds_read_b128 v[6:9], v14 offset:1024
	ds_read_b128 v[10:13], v14 offset:2048
	ds_read_b128 v[14:17], v14 offset:3072
	v_mov_b32_e32 v18, v201
	v_mov_b32_e32 v19, v202
	s_add_i32 m0, s43, 0xc000
	s_waitcnt lgkmcnt(0)
	ds_read_b128 v[58:61], v205
	ds_read_b128 v[62:65], v205 offset:1024
	ds_read_b128 v[50:53], v205 offset:2048
	ds_read_b128 v[54:57], v205 offset:3072
	ds_read_b128 v[42:45], v205 offset:4096
	ds_read_b128 v[46:49], v205 offset:5120
	ds_read_b128 v[34:37], v205 offset:6144
	ds_read_b128 v[38:41], v205 offset:7168
	s_andn2_b64 vcc, exec, s[30:31]
	global_load_lds_dwordx4 v18, s[4:5]
	s_add_i32 m0, s43, 0xe000
	v_cndmask_b32_e64 v18, 0, 1, s[30:31]
	global_load_lds_dwordx4 v19, s[4:5]
	s_waitcnt lgkmcnt(8)
	s_barrier
	s_waitcnt lgkmcnt(0)
	v_cmp_ne_u32_e64 s[6:7], 1, v18
	s_cbranch_vccnz .LBB0_1359
	s_nop 0
	s_waitcnt lgkmcnt(0)
	v_mfma_scale_f32_16x16x128_f8f6f4 v[98:101], v[2:9], v[58:65], v[98:101], v203, v203 op_sel_hi:[0,0,0]
	v_mfma_scale_f32_16x16x128_f8f6f4 v[94:97], v[10:17], v[58:65], v[94:97], v203, v203 op_sel_hi:[0,0,0]
	v_mfma_scale_f32_16x16x128_f8f6f4 v[90:93], v[2:9], v[50:57], v[90:93], v203, v203 op_sel_hi:[0,0,0]
	v_mfma_scale_f32_16x16x128_f8f6f4 v[86:89], v[10:17], v[50:57], v[86:89], v203, v203 op_sel_hi:[0,0,0]
	v_mfma_scale_f32_16x16x128_f8f6f4 v[82:85], v[2:9], v[42:49], v[82:85], v203, v203 op_sel_hi:[0,0,0]
	v_mfma_scale_f32_16x16x128_f8f6f4 v[78:81], v[10:17], v[42:49], v[78:81], v203, v203 op_sel_hi:[0,0,0]
	v_mfma_scale_f32_16x16x128_f8f6f4 v[74:77], v[2:9], v[34:41], v[74:77], v203, v203 op_sel_hi:[0,0,0]
	v_mfma_scale_f32_16x16x128_f8f6f4 v[70:73], v[10:17], v[34:41], v[70:73], v203, v203 op_sel_hi:[0,0,0]
	s_nop 0
.LBB0_1359:
	s_barrier
	s_mov_b32 m0, s44
	v_add_u32_e32 v30, 0x14000, v204
	v_mov_b32_e32 v66, v1
	v_mov_b32_e32 v68, v198
	ds_read_b128 v[18:21], v30
	ds_read_b128 v[22:25], v30 offset:1024
	ds_read_b128 v[26:29], v30 offset:2048
	ds_read_b128 v[30:33], v30 offset:3072
	s_and_b64 vcc, exec, s[6:7]
	global_load_lds_dwordx4 v66, s[36:37]
	s_mov_b32 m0, s45
	s_nop 0
	global_load_lds_dwordx4 v68, s[36:37]
	s_barrier
	s_waitcnt lgkmcnt(0)
	s_cbranch_vccnz .LBB0_1361
	s_nop 0
	s_waitcnt lgkmcnt(0)
	v_mfma_scale_f32_16x16x128_f8f6f4 v[130:133], v[18:25], v[58:65], v[130:133], v203, v203 op_sel_hi:[0,0,0]
	v_mfma_scale_f32_16x16x128_f8f6f4 v[126:129], v[26:33], v[58:65], v[126:129], v203, v203 op_sel_hi:[0,0,0]
	v_mfma_scale_f32_16x16x128_f8f6f4 v[122:125], v[18:25], v[50:57], v[122:125], v203, v203 op_sel_hi:[0,0,0]
	v_mfma_scale_f32_16x16x128_f8f6f4 v[118:121], v[26:33], v[50:57], v[118:121], v203, v203 op_sel_hi:[0,0,0]
	v_mfma_scale_f32_16x16x128_f8f6f4 v[114:117], v[18:25], v[42:49], v[114:117], v203, v203 op_sel_hi:[0,0,0]
	v_mfma_scale_f32_16x16x128_f8f6f4 v[110:113], v[26:33], v[42:49], v[110:113], v203, v203 op_sel_hi:[0,0,0]
	v_mfma_scale_f32_16x16x128_f8f6f4 v[106:109], v[18:25], v[34:41], v[106:109], v203, v203 op_sel_hi:[0,0,0]
	v_mfma_scale_f32_16x16x128_f8f6f4 v[102:105], v[26:33], v[34:41], v[102:105], v203, v203 op_sel_hi:[0,0,0]
	s_nop 0
.LBB0_1361:
	s_mov_b32 m0, s43
	v_mov_b32_e32 v66, v199
	v_mov_b32_e32 v68, v200
	s_barrier
	s_waitcnt lgkmcnt(0)
	ds_read_b128 v[58:61], v205 offset:16384
	ds_read_b128 v[62:65], v205 offset:17408
	ds_read_b128 v[50:53], v205 offset:18432
	ds_read_b128 v[54:57], v205 offset:19456
	ds_read_b128 v[42:45], v205 offset:20480
	ds_read_b128 v[46:49], v205 offset:21504
	ds_read_b128 v[34:37], v205 offset:22528
	ds_read_b128 v[38:41], v205 offset:23552
	s_andn2_b64 vcc, exec, s[34:35]
	global_load_lds_dwordx4 v66, s[38:39]
	s_mov_b32 m0, s46
	v_cndmask_b32_e64 v66, 0, 1, s[34:35]
	global_load_lds_dwordx4 v68, s[38:39]
	s_barrier
	s_waitcnt lgkmcnt(0)
	v_cmp_ne_u32_e64 s[4:5], 1, v66
	s_cbranch_vccnz .LBB0_1363
	s_nop 0
	s_waitcnt lgkmcnt(0)
	v_mfma_scale_f32_16x16x128_f8f6f4 v[162:165], v[2:9], v[58:65], v[162:165], v203, v203 op_sel_hi:[0,0,0]
	v_mfma_scale_f32_16x16x128_f8f6f4 v[158:161], v[10:17], v[58:65], v[158:161], v203, v203 op_sel_hi:[0,0,0]
	v_mfma_scale_f32_16x16x128_f8f6f4 v[154:157], v[2:9], v[50:57], v[154:157], v203, v203 op_sel_hi:[0,0,0]
	v_mfma_scale_f32_16x16x128_f8f6f4 v[150:153], v[10:17], v[50:57], v[150:153], v203, v203 op_sel_hi:[0,0,0]
	v_mfma_scale_f32_16x16x128_f8f6f4 v[146:149], v[2:9], v[42:49], v[146:149], v203, v203 op_sel_hi:[0,0,0]
	v_mfma_scale_f32_16x16x128_f8f6f4 v[142:145], v[10:17], v[42:49], v[142:145], v203, v203 op_sel_hi:[0,0,0]
	v_mfma_scale_f32_16x16x128_f8f6f4 v[138:141], v[2:9], v[34:41], v[138:141], v203, v203 op_sel_hi:[0,0,0]
	v_mfma_scale_f32_16x16x128_f8f6f4 v[134:137], v[10:17], v[34:41], v[134:137], v203, v203 op_sel_hi:[0,0,0]
	s_nop 0
; #define G8_STAGE(bufoff, gbase, v0, v1) do { unsigned x0_ = (v0), x1_ = (v1); asm volatile("" : "+v"(x0_), "+v"(x1_));     \
;         __builtin_amdgcn_global_load_lds((const unsigned*)((gbase) + x0_), (LAS unsigned*)(lds + (bufoff) + ldsw), 16, 0, 0); \
;         __builtin_amdgcn_global_load_lds((const unsigned*)((gbase) + x1_), (LAS unsigned*)(lds + (bufoff) + ldsw + 8192), 16, 0, 0); } while (0)
; #define G8_LDA(dst, b, h) do { _Pragma("unroll") for (int m = 0; m < 4; ++m) _Pragma("unroll") for (int k = 0; k < 2; ++k) dst[m][k] = *(const LAS bf16x8*)(lds + G8_SA(b, h) + aoff + m * 2048 + k * 1024); } while (0)
; #define G8_LDB(dst, b, h) do { _Pragma("unroll") for (int n = 0; n < 2; ++n) _Pragma("unroll") for (int k = 0; k < 2; ++k) dst[n][k] = *(const LAS bf16x8*)(lds + G8_SB(b, h) + boff + n * 2048 + k * 1024); } while (0)
; #define G8_WAIT_V(n) asm volatile("s_waitcnt vmcnt(" #n ")" ::: "memory")
; #define G8_WAIT_L(n) asm volatile("s_waitcnt lgkmcnt(" #n ")" ::: "memory")
; #define G8_BAR __builtin_amdgcn_s_barrier()
; #define G8_SCHED __builtin_amdgcn_sched_barrier(0)
;     ...
;             G8_STAGE(G8_SB(0, 1), b2 + hstepB, voffB[0], voffB[1]);
;             if constexpr (CONV) G8_WAIT_V(9); else G8_WAIT_V(6);
;             G8_BAR; if (do1) G8_MMA(1, 1, At, B1); G8_BAR;
;             G8_LDB(B0, 1, 0); G8_SCHED; G8_LDA(At, 1, 0); G8_STAGE(G8_SA(0, 1), a2, o10, o11);
;             G8_WAIT_L(8); G8_BAR; G8_WAIT_L(0); if (do0) G8_MMA(0, 0, At, B0); G8_BAR; G8_SCHED;
;             G8_LDB(B1, 1, 1); G8_STAGE(G8_SB(1, 0), b3, voffB[0], voffB[1]);
;             G8_BAR; G8_WAIT_L(0); if (do0) G8_MMA(0, 1, At, B1); G8_BAR;
.LBB0_1363:
	s_barrier
	s_add_u32 s76, s36, 0x4000
	s_mov_b32 m0, s47
	v_mov_b32_e32 v2, v1
	v_mov_b32_e32 v3, v198
	s_addc_u32 s77, s37, 0
	s_and_b64 vcc, exec, s[4:5]
	global_load_lds_dwordx4 v2, s[76:77]
	s_mov_b32 m0, s48
	s_nop 0
	global_load_lds_dwordx4 v3, s[76:77]
	s_waitcnt vmcnt(6)
	s_barrier
	s_cbranch_vccnz .LBB0_1365
	s_nop 0
	s_waitcnt lgkmcnt(0)
	v_mfma_scale_f32_16x16x128_f8f6f4 v[194:197], v[18:25], v[58:65], v[194:197], v203, v203 op_sel_hi:[0,0,0]
	v_mfma_scale_f32_16x16x128_f8f6f4 v[190:193], v[26:33], v[58:65], v[190:193], v203, v203 op_sel_hi:[0,0,0]
	v_mfma_scale_f32_16x16x128_f8f6f4 v[186:189], v[18:25], v[50:57], v[186:189], v203, v203 op_sel_hi:[0,0,0]
	v_mfma_scale_f32_16x16x128_f8f6f4 v[182:185], v[26:33], v[50:57], v[182:185], v203, v203 op_sel_hi:[0,0,0]
	v_mfma_scale_f32_16x16x128_f8f6f4 v[178:181], v[18:25], v[42:49], v[178:181], v203, v203 op_sel_hi:[0,0,0]
	v_mfma_scale_f32_16x16x128_f8f6f4 v[174:177], v[26:33], v[42:49], v[174:177], v203, v203 op_sel_hi:[0,0,0]
	v_mfma_scale_f32_16x16x128_f8f6f4 v[170:173], v[18:25], v[34:41], v[170:173], v203, v203 op_sel_hi:[0,0,0]
	v_mfma_scale_f32_16x16x128_f8f6f4 v[166:169], v[26:33], v[34:41], v[166:169], v203, v203 op_sel_hi:[0,0,0]
	s_nop 0
.LBB0_1365:
	v_add_u32_e32 v14, 0x18000, v204
	s_barrier
	ds_read_b128 v[2:5], v14
	ds_read_b128 v[6:9], v14 offset:1024
	ds_read_b128 v[10:13], v14 offset:2048
	ds_read_b128 v[14:17], v14 offset:3072
	s_mov_b32 m0, s49
	v_mov_b32_e32 v18, v201
	v_mov_b32_e32 v19, v202
	s_waitcnt lgkmcnt(0)
	ds_read_b128 v[58:61], v205 offset:32768
	ds_read_b128 v[62:65], v205 offset:33792
	ds_read_b128 v[50:53], v205 offset:34816
	ds_read_b128 v[54:57], v205 offset:35840
	ds_read_b128 v[42:45], v205 offset:36864
	ds_read_b128 v[46:49], v205 offset:37888
	ds_read_b128 v[34:37], v205 offset:38912
	ds_read_b128 v[38:41], v205 offset:39936
	s_and_b64 vcc, exec, s[6:7]
	global_load_lds_dwordx4 v18, s[38:39]
	s_mov_b32 m0, s50
	s_nop 0
	global_load_lds_dwordx4 v19, s[38:39]
	s_waitcnt lgkmcnt(8)
	s_barrier
	s_waitcnt lgkmcnt(0)
	s_cbranch_vccnz .LBB0_1367
	s_nop 0
	s_waitcnt lgkmcnt(0)
	v_mfma_scale_f32_16x16x128_f8f6f4 v[98:101], v[2:9], v[58:65], v[98:101], v203, v203 op_sel_hi:[0,0,0]
	v_mfma_scale_f32_16x16x128_f8f6f4 v[94:97], v[10:17], v[58:65], v[94:97], v203, v203 op_sel_hi:[0,0,0]
	v_mfma_scale_f32_16x16x128_f8f6f4 v[90:93], v[2:9], v[50:57], v[90:93], v203, v203 op_sel_hi:[0,0,0]
	v_mfma_scale_f32_16x16x128_f8f6f4 v[86:89], v[10:17], v[50:57], v[86:89], v203, v203 op_sel_hi:[0,0,0]
	v_mfma_scale_f32_16x16x128_f8f6f4 v[82:85], v[2:9], v[42:49], v[82:85], v203, v203 op_sel_hi:[0,0,0]
	v_mfma_scale_f32_16x16x128_f8f6f4 v[78:81], v[10:17], v[42:49], v[78:81], v203, v203 op_sel_hi:[0,0,0]
	v_mfma_scale_f32_16x16x128_f8f6f4 v[74:77], v[2:9], v[34:41], v[74:77], v203, v203 op_sel_hi:[0,0,0]
	v_mfma_scale_f32_16x16x128_f8f6f4 v[70:73], v[10:17], v[34:41], v[70:73], v203, v203 op_sel_hi:[0,0,0]
	s_nop 0
.LBB0_1367:
	s_add_u32 s76, s36, 0x8000
	s_addc_u32 s77, s37, 0
	s_barrier
	s_mov_b32 m0, s53
	v_add_u32_e32 v30, 0x1c000, v204
	v_mov_b32_e32 v66, v198
	v_mov_b32_e32 v68, v1
	ds_read_b128 v[18:21], v30
	ds_read_b128 v[22:25], v30 offset:1024
	ds_read_b128 v[26:29], v30 offset:2048
	ds_read_b128 v[30:33], v30 offset:3072
	s_and_b64 vcc, exec, s[6:7]
	global_load_lds_dwordx4 v68, s[76:77]
	s_mov_b32 m0, s54
	s_nop 0
	global_load_lds_dwordx4 v66, s[76:77]
	s_barrier
	s_waitcnt lgkmcnt(0)
	s_cbranch_vccnz .LBB0_1369
	s_nop 0
	s_waitcnt lgkmcnt(0)
	v_mfma_scale_f32_16x16x128_f8f6f4 v[130:133], v[18:25], v[58:65], v[130:133], v203, v203 op_sel_hi:[0,0,0]
	v_mfma_scale_f32_16x16x128_f8f6f4 v[126:129], v[26:33], v[58:65], v[126:129], v203, v203 op_sel_hi:[0,0,0]
	v_mfma_scale_f32_16x16x128_f8f6f4 v[122:125], v[18:25], v[50:57], v[122:125], v203, v203 op_sel_hi:[0,0,0]
	v_mfma_scale_f32_16x16x128_f8f6f4 v[118:121], v[26:33], v[50:57], v[118:121], v203, v203 op_sel_hi:[0,0,0]
	v_mfma_scale_f32_16x16x128_f8f6f4 v[114:117], v[18:25], v[42:49], v[114:117], v203, v203 op_sel_hi:[0,0,0]
	v_mfma_scale_f32_16x16x128_f8f6f4 v[110:113], v[26:33], v[42:49], v[110:113], v203, v203 op_sel_hi:[0,0,0]
	v_mfma_scale_f32_16x16x128_f8f6f4 v[106:109], v[18:25], v[34:41], v[106:109], v203, v203 op_sel_hi:[0,0,0]
	v_mfma_scale_f32_16x16x128_f8f6f4 v[102:105], v[26:33], v[34:41], v[102:105], v203, v203 op_sel_hi:[0,0,0]
	s_nop 0
; #define G8_STAGE(bufoff, gbase, v0, v1) do { unsigned x0_ = (v0), x1_ = (v1); asm volatile("" : "+v"(x0_), "+v"(x1_));     \
;         __builtin_amdgcn_global_load_lds((const unsigned*)((gbase) + x0_), (LAS unsigned*)(lds + (bufoff) + ldsw), 16, 0, 0); \
;         __builtin_amdgcn_global_load_lds((const unsigned*)((gbase) + x1_), (LAS unsigned*)(lds + (bufoff) + ldsw + 8192), 16, 0, 0); } while (0)
; #define G8_LDA(dst, b, h) do { _Pragma("unroll") for (int m = 0; m < 4; ++m) _Pragma("unroll") for (int k = 0; k < 2; ++k) dst[m][k] = *(const LAS bf16x8*)(lds + G8_SA(b, h) + aoff + m * 2048 + k * 1024); } while (0)
; #define G8_WAIT_V(n) asm volatile("s_waitcnt vmcnt(" #n ")" ::: "memory")
; #define G8_WAIT_L(n) asm volatile("s_waitcnt lgkmcnt(" #n ")" ::: "memory")
; #define G8_BAR __builtin_amdgcn_s_barrier()
; #define G8_SCHED __builtin_amdgcn_sched_barrier(0)
;     ...
;             G8_LDA(At, 1, 1); G8_STAGE(G8_SA(1, 0), a3, o00, o01);
;             G8_BAR; G8_WAIT_L(0); if (do1) G8_MMA(1, 0, At, B0); G8_BAR; G8_SCHED;
;             G8_STAGE(G8_SB(1, 1), b3 + hstepB, voffB[0], voffB[1]);
;             G8_WAIT_V(6); G8_BAR; if (do1) G8_MMA(1, 1, At, B1); G8_BAR;
.LBB0_1369:
	v_mov_b32_e32 v66, v199
	v_mov_b32_e32 v68, v200
	s_barrier
	s_waitcnt lgkmcnt(0)
	ds_read_b128 v[58:61], v205 offset:49152
	ds_read_b128 v[62:65], v205 offset:50176
	ds_read_b128 v[50:53], v205 offset:51200
	ds_read_b128 v[54:57], v205 offset:52224
	ds_read_b128 v[42:45], v205 offset:53248
	ds_read_b128 v[46:49], v205 offset:54272
	ds_read_b128 v[34:37], v205 offset:55296
	ds_read_b128 v[38:41], v205 offset:56320
	v_mov_b32_e32 v69, v67
	v_lshl_add_u64 v[206:207], s[38:39], 0, v[66:67]
	s_mov_b32 m0, s55
	v_lshl_add_u64 v[206:207], v[206:207], 0, s[12:13]
	v_lshl_add_u64 v[68:69], s[38:39], 0, v[68:69]
	global_load_lds_dwordx4 v[206:207], off
	v_lshl_add_u64 v[68:69], v[68:69], 0, s[12:13]
	s_mov_b32 m0, s56
	s_and_b64 vcc, exec, s[4:5]
	global_load_lds_dwordx4 v[68:69], off
	s_barrier
	s_waitcnt lgkmcnt(0)
	s_cbranch_vccnz .LBB0_1371
	s_nop 0
	s_waitcnt lgkmcnt(0)
	v_mfma_scale_f32_16x16x128_f8f6f4 v[162:165], v[2:9], v[58:65], v[162:165], v203, v203 op_sel_hi:[0,0,0]
	v_mfma_scale_f32_16x16x128_f8f6f4 v[158:161], v[10:17], v[58:65], v[158:161], v203, v203 op_sel_hi:[0,0,0]
	v_mfma_scale_f32_16x16x128_f8f6f4 v[154:157], v[2:9], v[50:57], v[154:157], v203, v203 op_sel_hi:[0,0,0]
	v_mfma_scale_f32_16x16x128_f8f6f4 v[150:153], v[10:17], v[50:57], v[150:153], v203, v203 op_sel_hi:[0,0,0]
	v_mfma_scale_f32_16x16x128_f8f6f4 v[146:149], v[2:9], v[42:49], v[146:149], v203, v203 op_sel_hi:[0,0,0]
	v_mfma_scale_f32_16x16x128_f8f6f4 v[142:145], v[10:17], v[42:49], v[142:145], v203, v203 op_sel_hi:[0,0,0]
	v_mfma_scale_f32_16x16x128_f8f6f4 v[138:141], v[2:9], v[34:41], v[138:141], v203, v203 op_sel_hi:[0,0,0]
	v_mfma_scale_f32_16x16x128_f8f6f4 v[134:137], v[10:17], v[34:41], v[134:137], v203, v203 op_sel_hi:[0,0,0]
	s_nop 0
.LBB0_1371:
	s_barrier
	s_add_u32 s6, s36, 0xc000
	s_mov_b32 m0, s57
	v_mov_b32_e32 v2, v1
	v_mov_b32_e32 v3, v198
	s_addc_u32 s7, s37, 0
	s_and_b64 vcc, exec, s[4:5]
	global_load_lds_dwordx4 v2, s[6:7]
	s_mov_b32 m0, s58
	s_nop 0
	global_load_lds_dwordx4 v3, s[6:7]
	s_waitcnt vmcnt(6)
	s_barrier
	s_cbranch_vccnz .LBB0_1356
	s_nop 0
	s_waitcnt lgkmcnt(0)
	v_mfma_scale_f32_16x16x128_f8f6f4 v[194:197], v[18:25], v[58:65], v[194:197], v203, v203 op_sel_hi:[0,0,0]
	v_mfma_scale_f32_16x16x128_f8f6f4 v[190:193], v[26:33], v[58:65], v[190:193], v203, v203 op_sel_hi:[0,0,0]
	v_mfma_scale_f32_16x16x128_f8f6f4 v[186:189], v[18:25], v[50:57], v[186:189], v203, v203 op_sel_hi:[0,0,0]
	v_mfma_scale_f32_16x16x128_f8f6f4 v[182:185], v[26:33], v[50:57], v[182:185], v203, v203 op_sel_hi:[0,0,0]
	v_mfma_scale_f32_16x16x128_f8f6f4 v[178:181], v[18:25], v[42:49], v[178:181], v203, v203 op_sel_hi:[0,0,0]
	v_mfma_scale_f32_16x16x128_f8f6f4 v[174:177], v[26:33], v[42:49], v[174:177], v203, v203 op_sel_hi:[0,0,0]
	v_mfma_scale_f32_16x16x128_f8f6f4 v[170:173], v[18:25], v[34:41], v[170:173], v203, v203 op_sel_hi:[0,0,0]
	v_mfma_scale_f32_16x16x128_f8f6f4 v[166:169], v[26:33], v[34:41], v[166:169], v203, v203 op_sel_hi:[0,0,0]
	s_nop 0
	s_branch .LBB0_1356
